# attention per-item overheads: row-sum LDS reads batched in the epilogues, active test on SCC, next-item pull ahead of the epilogue (on top of v35)
# speedup vs baseline: 1.0057x; 1.0057x over previous
; #define LDS_WAIT() asm volatile("s_waitcnt lgkmcnt(0)" ::: "memory")
; __device__ __forceinline__ unsigned cvt4_fp8(float a, float b, float c, float d) { int w = 0; w = __builtin_amdgcn_cvt_pk_fp8_f32(a, b, w, false); w = __builtin_amdgcn_cvt_pk_fp8_f32(c, d, w, true); return (unsigned)w; }
; template <bool MLA>
; __device__ __forceinline__ void attn_unit(char* lds, int h, int qb, const bf16_t* Qp, int ldq, const bf16_t* Kp, int ldk, const bf16_t* KRp, const bf16_t* Vp, int ldv,
;                                           unsigned char* Op, int ldo, const float* KMp, const float* rel_bias) {
;     ...
;     if (hi == 0) li_l[r32] = l_reg; LDS_WAIT();
;     unsigned char* Ow = Op + (size_t)qlo * ldo;
; #pragma unroll
;     for (int r = 0; r < 16; ++r) { const int orow = CROWC(r) + 4 * hi; const float rl = 16.0f * __builtin_amdgcn_rcpf(li_h[CROWC(r)]);
; #pragma unroll
;         for (int d0 = 0; d0 < 4; ++d0) { const float v = o[d0][r] * rl; const float v1 = __shfl_xor(v, 1), v2 = __shfl_xor(v, 2), v3 = __shfl_xor(v1, 2);
;             if ((r32 & 3) == 0) *(unsigned*)(Ow + (size_t)orow * ldo + d0 * 32 + r32) = cvt4_fp8(v, v1, v2, v3); } }
; __global__ void __launch_bounds__(512, 2) mega_fwd(Args args) {
;     ...
;         for (;;) { if (tid == 0) MISC[12] = atomicAdd(ctl + CW_AQ1, 1u);
;             __syncthreads(); const int it = (int)MISC[12]; __syncthreads();
.LBB0_1394:
	s_mov_b64 s[98:99], exec
	s_and_b64 exec, exec, s[14:15]
	v_mov_b32_e32 v254, 0
	v_mov_b32_e32 v253, 1
	s_nop 0
	global_atomic_add v253, v254, v253, s[8:9] sc0
	s_mov_b64 exec, s[98:99]
	s_and_saveexec_b64 s[44:45], s[4:5]
	ds_write_b32 v173, v178
	s_or_b64 exec, exec, s[44:45]
	s_waitcnt lgkmcnt(0)
	ds_read_b32 v66, v167
	ds_read_b32 v234, v167 offset:4
	ds_read_b32 v235, v167 offset:8
	ds_read_b32 v236, v167 offset:12
	ds_read_b32 v237, v167 offset:32
	ds_read_b32 v238, v167 offset:36
	ds_read_b32 v239, v167 offset:40
	ds_read_b32 v240, v167 offset:44
	ds_read_b32 v241, v167 offset:64
	ds_read_b32 v242, v167 offset:68
	ds_read_b32 v243, v167 offset:72
	ds_read_b32 v244, v167 offset:76
	ds_read_b32 v245, v167 offset:96
	ds_read_b32 v246, v167 offset:100
	ds_read_b32 v247, v167 offset:104
	ds_read_b32 v248, v167 offset:108
	v_and_b32_e32 v68, 64, v195
	v_xor_b32_e32 v67, 1, v195
	v_add_u32_e32 v72, 64, v68
	v_cmp_lt_i32_e32 vcc, v67, v72
	s_waitcnt lgkmcnt(0)
	v_rcp_f32_e32 v66, v66
	s_lshl_b32 s10, s27, 7
	v_cndmask_b32_e32 v67, v195, v67, vcc
	v_lshlrev_b32_e32 v68, 2, v67
	v_mul_f32_e32 v69, 0x41800000, v66
	v_mul_f32_e32 v70, v34, v69
	s_nop 1
	v_mov_b32_dpp v71, v70 quad_perm:[1,0,3,2] row_mask:0xf bank_mask:0xf
	v_xor_b32_e32 v67, 2, v195
	s_add_u32 s22, s70, s43
	v_cmp_lt_i32_e32 vcc, v67, v72
	s_addc_u32 s23, s71, 0
	s_add_u32 s10, s22, s10
	v_cndmask_b32_e32 v34, v195, v67, vcc
	s_mov_b32 s43, s11
	v_lshlrev_b32_e32 v34, 2, v34
	s_addc_u32 s22, s23, 0
	s_lshl_b64 s[42:43], s[42:43], 11
	s_nop 1
	v_mov_b32_dpp v72, v70 quad_perm:[2,3,0,1] row_mask:0xf bank_mask:0xf
	s_waitcnt lgkmcnt(0)
	s_nop 1
	v_mov_b32_dpp v73, v71 quad_perm:[2,3,0,1] row_mask:0xf bank_mask:0xf
	s_add_u32 s42, s10, s42
	s_addc_u32 s43, s22, s43
	v_lshl_add_u64 v[66:67], s[42:43], 0, v[168:169]
	v_lshl_add_u64 v[66:67], v[66:67], 0, v[170:171]
	s_and_saveexec_b64 s[42:43], s[6:7]
	s_cbranch_execz .LBB0_1398
	v_mov_b32_e32 v74, v147
	v_cvt_pk_fp8_f32 v74, v70, v71
	s_waitcnt lgkmcnt(0)
	v_cvt_pk_fp8_f32 v74, v72, v73 op_sel:[0,0,1]
	global_store_dword v[66:67], v74, off

; __device__ __forceinline__ unsigned cvt4_fp8(float a, float b, float c, float d) { int w = 0; w = __builtin_amdgcn_cvt_pk_fp8_f32(a, b, w, false); w = __builtin_amdgcn_cvt_pk_fp8_f32(c, d, w, true); return (unsigned)w; }
; template <bool MLA>
; __device__ __forceinline__ void attn_unit(char* lds, int h, int qb, const bf16_t* Qp, int ldq, const bf16_t* Kp, int ldk, const bf16_t* KRp, const bf16_t* Vp, int ldv,
;                                           unsigned char* Op, int ldo, const float* KMp, const float* rel_bias) {
;     ...
;     for (int r = 0; r < 16; ++r) { const int orow = CROWC(r) + 4 * hi; const float rl = 16.0f * __builtin_amdgcn_rcpf(li_h[CROWC(r)]);
; #pragma unroll
;         for (int d0 = 0; d0 < 4; ++d0) { const float v = o[d0][r] * rl; const float v1 = __shfl_xor(v, 1), v2 = __shfl_xor(v, 2), v3 = __shfl_xor(v1, 2);
;             if ((r32 & 3) == 0) *(unsigned*)(Ow + (size_t)orow * ldo + d0 * 32 + r32) = cvt4_fp8(v, v1, v2, v3); } }
.LBB0_1404:
	s_or_b64 exec, exec, s[42:43]
	v_mov_b32_e32 v2, v234
	v_rcp_f32_e32 v2, v2
	s_nop 0
	v_mul_f32_e32 v2, 0x41800000, v2
	v_mul_f32_e32 v18, v35, v2
	s_nop 1
	v_mov_b32_dpp v50, v18 quad_perm:[1,0,3,2] row_mask:0xf bank_mask:0xf
	s_nop 1
	v_mov_b32_dpp v35, v18 quad_perm:[2,3,0,1] row_mask:0xf bank_mask:0xf
	s_waitcnt lgkmcnt(0)
	s_nop 1
	v_mov_b32_dpp v69, v50 quad_perm:[2,3,0,1] row_mask:0xf bank_mask:0xf
	s_and_saveexec_b64 s[42:43], s[6:7]
	s_cbranch_execz .LBB0_1406
	v_mov_b32_e32 v70, v147
	v_cvt_pk_fp8_f32 v70, v18, v50
	s_waitcnt lgkmcnt(0)
	v_cvt_pk_fp8_f32 v70, v35, v69 op_sel:[0,0,1]
	global_store_dword v[66:67], v70, off offset:2048

; __device__ __forceinline__ unsigned cvt4_fp8(float a, float b, float c, float d) { int w = 0; w = __builtin_amdgcn_cvt_pk_fp8_f32(a, b, w, false); w = __builtin_amdgcn_cvt_pk_fp8_f32(c, d, w, true); return (unsigned)w; }
; template <bool MLA>
; __device__ __forceinline__ void attn_unit(char* lds, int h, int qb, const bf16_t* Qp, int ldq, const bf16_t* Kp, int ldk, const bf16_t* KRp, const bf16_t* Vp, int ldv,
;                                           unsigned char* Op, int ldo, const float* KMp, const float* rel_bias) {
;     ...
;     for (int r = 0; r < 16; ++r) { const int orow = CROWC(r) + 4 * hi; const float rl = 16.0f * __builtin_amdgcn_rcpf(li_h[CROWC(r)]);
; #pragma unroll
;         for (int d0 = 0; d0 < 4; ++d0) { const float v = o[d0][r] * rl; const float v1 = __shfl_xor(v, 1), v2 = __shfl_xor(v, 2), v3 = __shfl_xor(v1, 2);
;             if ((r32 & 3) == 0) *(unsigned*)(Ow + (size_t)orow * ldo + d0 * 32 + r32) = cvt4_fp8(v, v1, v2, v3); } }
.LBB0_1412:
	s_or_b64 exec, exec, s[42:43]
	v_mov_b32_e32 v2, v235
	v_rcp_f32_e32 v2, v2
	s_nop 0
	v_mul_f32_e32 v2, 0x41800000, v2
	v_mul_f32_e32 v3, v36, v2
	s_nop 1
	v_mov_b32_dpp v19, v3 quad_perm:[1,0,3,2] row_mask:0xf bank_mask:0xf
	s_nop 1
	v_mov_b32_dpp v18, v3 quad_perm:[2,3,0,1] row_mask:0xf bank_mask:0xf
	s_waitcnt lgkmcnt(0)
	s_nop 1
	v_mov_b32_dpp v35, v19 quad_perm:[2,3,0,1] row_mask:0xf bank_mask:0xf
	s_and_saveexec_b64 s[42:43], s[6:7]
	s_cbranch_execz .LBB0_1414
	v_mov_b32_e32 v36, v147
	v_cvt_pk_fp8_f32 v36, v3, v19
	s_waitcnt lgkmcnt(0)
	v_cvt_pk_fp8_f32 v36, v18, v35 op_sel:[0,0,1]
	v_add_co_u32_e32 v18, vcc, 0x1000, v66
	s_nop 1
	v_addc_co_u32_e32 v19, vcc, 0, v67, vcc
	global_store_dword v[18:19], v36, off

; __device__ __forceinline__ unsigned cvt4_fp8(float a, float b, float c, float d) { int w = 0; w = __builtin_amdgcn_cvt_pk_fp8_f32(a, b, w, false); w = __builtin_amdgcn_cvt_pk_fp8_f32(c, d, w, true); return (unsigned)w; }
; template <bool MLA>
; __device__ __forceinline__ void attn_unit(char* lds, int h, int qb, const bf16_t* Qp, int ldq, const bf16_t* Kp, int ldk, const bf16_t* KRp, const bf16_t* Vp, int ldv,
;                                           unsigned char* Op, int ldo, const float* KMp, const float* rel_bias) {
;     ...
;     for (int r = 0; r < 16; ++r) { const int orow = CROWC(r) + 4 * hi; const float rl = 16.0f * __builtin_amdgcn_rcpf(li_h[CROWC(r)]);
; #pragma unroll
;         for (int d0 = 0; d0 < 4; ++d0) { const float v = o[d0][r] * rl; const float v1 = __shfl_xor(v, 1), v2 = __shfl_xor(v, 2), v3 = __shfl_xor(v1, 2);
;             if ((r32 & 3) == 0) *(unsigned*)(Ow + (size_t)orow * ldo + d0 * 32 + r32) = cvt4_fp8(v, v1, v2, v3); } }
.LBB0_1420:
	s_or_b64 exec, exec, s[42:43]
	v_mov_b32_e32 v2, v236
	v_rcp_f32_e32 v2, v2
	s_nop 0
	v_mul_f32_e32 v2, 0x41800000, v2
	v_mul_f32_e32 v3, v37, v2
	s_nop 1
	v_mov_b32_dpp v18, v3 quad_perm:[1,0,3,2] row_mask:0xf bank_mask:0xf
	s_nop 1
	v_mov_b32_dpp v4, v3 quad_perm:[2,3,0,1] row_mask:0xf bank_mask:0xf
	s_waitcnt lgkmcnt(0)
	s_nop 1
	v_mov_b32_dpp v19, v18 quad_perm:[2,3,0,1] row_mask:0xf bank_mask:0xf
	s_and_saveexec_b64 s[42:43], s[6:7]
	s_cbranch_execz .LBB0_1422
	v_mov_b32_e32 v20, v147
	v_cvt_pk_fp8_f32 v20, v3, v18
	v_add_co_u32_e32 v18, vcc, 0x1000, v66
	s_waitcnt lgkmcnt(0)
	v_cvt_pk_fp8_f32 v20, v4, v19 op_sel:[0,0,1]
	v_addc_co_u32_e32 v19, vcc, 0, v67, vcc
	global_store_dword v[18:19], v20, off offset:2048

; __device__ __forceinline__ unsigned cvt4_fp8(float a, float b, float c, float d) { int w = 0; w = __builtin_amdgcn_cvt_pk_fp8_f32(a, b, w, false); w = __builtin_amdgcn_cvt_pk_fp8_f32(c, d, w, true); return (unsigned)w; }
; template <bool MLA>
; __device__ __forceinline__ void attn_unit(char* lds, int h, int qb, const bf16_t* Qp, int ldq, const bf16_t* Kp, int ldk, const bf16_t* KRp, const bf16_t* Vp, int ldv,
;                                           unsigned char* Op, int ldo, const float* KMp, const float* rel_bias) {
;     ...
;     for (int r = 0; r < 16; ++r) { const int orow = CROWC(r) + 4 * hi; const float rl = 16.0f * __builtin_amdgcn_rcpf(li_h[CROWC(r)]);
; #pragma unroll
;         for (int d0 = 0; d0 < 4; ++d0) { const float v = o[d0][r] * rl; const float v1 = __shfl_xor(v, 1), v2 = __shfl_xor(v, 2), v3 = __shfl_xor(v1, 2);
;             if ((r32 & 3) == 0) *(unsigned*)(Ow + (size_t)orow * ldo + d0 * 32 + r32) = cvt4_fp8(v, v1, v2, v3); } }
.LBB0_1428:
	s_or_b64 exec, exec, s[42:43]
	v_mov_b32_e32 v2, v237
	v_rcp_f32_e32 v2, v2
	s_nop 0
	v_mul_f32_e32 v2, 0x41800000, v2
	v_mul_f32_e32 v3, v38, v2
	s_nop 1
	v_mov_b32_dpp v5, v3 quad_perm:[1,0,3,2] row_mask:0xf bank_mask:0xf
	s_nop 1
	v_mov_b32_dpp v4, v3 quad_perm:[2,3,0,1] row_mask:0xf bank_mask:0xf
	s_waitcnt lgkmcnt(0)
	s_nop 1
	v_mov_b32_dpp v18, v5 quad_perm:[2,3,0,1] row_mask:0xf bank_mask:0xf
	s_and_saveexec_b64 s[42:43], s[6:7]
	s_cbranch_execz .LBB0_1430
	v_mov_b32_e32 v19, v147
	v_cvt_pk_fp8_f32 v19, v3, v5
	s_waitcnt lgkmcnt(0)
	v_cvt_pk_fp8_f32 v19, v4, v18 op_sel:[0,0,1]
	v_add_co_u32_e32 v4, vcc, 0x4000, v66
	s_nop 1
	v_addc_co_u32_e32 v5, vcc, 0, v67, vcc
	global_store_dword v[4:5], v19, off

; __device__ __forceinline__ unsigned cvt4_fp8(float a, float b, float c, float d) { int w = 0; w = __builtin_amdgcn_cvt_pk_fp8_f32(a, b, w, false); w = __builtin_amdgcn_cvt_pk_fp8_f32(c, d, w, true); return (unsigned)w; }
; template <bool MLA>
; __device__ __forceinline__ void attn_unit(char* lds, int h, int qb, const bf16_t* Qp, int ldq, const bf16_t* Kp, int ldk, const bf16_t* KRp, const bf16_t* Vp, int ldv,
;                                           unsigned char* Op, int ldo, const float* KMp, const float* rel_bias) {
;     ...
;     for (int r = 0; r < 16; ++r) { const int orow = CROWC(r) + 4 * hi; const float rl = 16.0f * __builtin_amdgcn_rcpf(li_h[CROWC(r)]);
; #pragma unroll
;         for (int d0 = 0; d0 < 4; ++d0) { const float v = o[d0][r] * rl; const float v1 = __shfl_xor(v, 1), v2 = __shfl_xor(v, 2), v3 = __shfl_xor(v1, 2);
;             if ((r32 & 3) == 0) *(unsigned*)(Ow + (size_t)orow * ldo + d0 * 32 + r32) = cvt4_fp8(v, v1, v2, v3); } }
.LBB0_1436:
	s_or_b64 exec, exec, s[42:43]
	v_mov_b32_e32 v2, v238
	v_rcp_f32_e32 v2, v2
	s_nop 0
	v_mul_f32_e32 v2, 0x41800000, v2
	v_mul_f32_e32 v3, v39, v2
	s_nop 1
	v_mov_b32_dpp v5, v3 quad_perm:[1,0,3,2] row_mask:0xf bank_mask:0xf
	s_nop 1
	v_mov_b32_dpp v4, v3 quad_perm:[2,3,0,1] row_mask:0xf bank_mask:0xf
	s_waitcnt lgkmcnt(0)
	s_nop 1
	v_mov_b32_dpp v6, v5 quad_perm:[2,3,0,1] row_mask:0xf bank_mask:0xf
	s_and_saveexec_b64 s[42:43], s[6:7]
	s_cbranch_execz .LBB0_1438
	v_mov_b32_e32 v18, v147
	v_cvt_pk_fp8_f32 v18, v3, v5
	s_waitcnt lgkmcnt(0)
	v_cvt_pk_fp8_f32 v18, v4, v6 op_sel:[0,0,1]
	v_add_co_u32_e32 v4, vcc, 0x4000, v66
	s_nop 1
	v_addc_co_u32_e32 v5, vcc, 0, v67, vcc
	global_store_dword v[4:5], v18, off offset:2048

; __device__ __forceinline__ unsigned cvt4_fp8(float a, float b, float c, float d) { int w = 0; w = __builtin_amdgcn_cvt_pk_fp8_f32(a, b, w, false); w = __builtin_amdgcn_cvt_pk_fp8_f32(c, d, w, true); return (unsigned)w; }
; template <bool MLA>
; __device__ __forceinline__ void attn_unit(char* lds, int h, int qb, const bf16_t* Qp, int ldq, const bf16_t* Kp, int ldk, const bf16_t* KRp, const bf16_t* Vp, int ldv,
;                                           unsigned char* Op, int ldo, const float* KMp, const float* rel_bias) {
;     ...
;     for (int r = 0; r < 16; ++r) { const int orow = CROWC(r) + 4 * hi; const float rl = 16.0f * __builtin_amdgcn_rcpf(li_h[CROWC(r)]);
; #pragma unroll
;         for (int d0 = 0; d0 < 4; ++d0) { const float v = o[d0][r] * rl; const float v1 = __shfl_xor(v, 1), v2 = __shfl_xor(v, 2), v3 = __shfl_xor(v1, 2);
;             if ((r32 & 3) == 0) *(unsigned*)(Ow + (size_t)orow * ldo + d0 * 32 + r32) = cvt4_fp8(v, v1, v2, v3); } }
.LBB0_1444:
	s_or_b64 exec, exec, s[42:43]
	v_mov_b32_e32 v2, v239
	v_rcp_f32_e32 v2, v2
	s_nop 0
	v_mul_f32_e32 v2, 0x41800000, v2
	v_mul_f32_e32 v3, v40, v2
	s_nop 1
	v_mov_b32_dpp v5, v3 quad_perm:[1,0,3,2] row_mask:0xf bank_mask:0xf
	s_nop 1
	v_mov_b32_dpp v4, v3 quad_perm:[2,3,0,1] row_mask:0xf bank_mask:0xf
	s_waitcnt lgkmcnt(0)
	s_nop 1
	v_mov_b32_dpp v6, v5 quad_perm:[2,3,0,1] row_mask:0xf bank_mask:0xf
	s_and_saveexec_b64 s[42:43], s[6:7]
	s_cbranch_execz .LBB0_1446
	v_mov_b32_e32 v7, v147
	v_cvt_pk_fp8_f32 v7, v3, v5
	s_waitcnt lgkmcnt(0)
	v_cvt_pk_fp8_f32 v7, v4, v6 op_sel:[0,0,1]
	v_add_co_u32_e32 v4, vcc, 0x5000, v66
	s_nop 1
	v_addc_co_u32_e32 v5, vcc, 0, v67, vcc
	global_store_dword v[4:5], v7, off

; __device__ __forceinline__ unsigned cvt4_fp8(float a, float b, float c, float d) { int w = 0; w = __builtin_amdgcn_cvt_pk_fp8_f32(a, b, w, false); w = __builtin_amdgcn_cvt_pk_fp8_f32(c, d, w, true); return (unsigned)w; }
; template <bool MLA>
; __device__ __forceinline__ void attn_unit(char* lds, int h, int qb, const bf16_t* Qp, int ldq, const bf16_t* Kp, int ldk, const bf16_t* KRp, const bf16_t* Vp, int ldv,
;                                           unsigned char* Op, int ldo, const float* KMp, const float* rel_bias) {
;     ...
;     for (int r = 0; r < 16; ++r) { const int orow = CROWC(r) + 4 * hi; const float rl = 16.0f * __builtin_amdgcn_rcpf(li_h[CROWC(r)]);
; #pragma unroll
;         for (int d0 = 0; d0 < 4; ++d0) { const float v = o[d0][r] * rl; const float v1 = __shfl_xor(v, 1), v2 = __shfl_xor(v, 2), v3 = __shfl_xor(v1, 2);
;             if ((r32 & 3) == 0) *(unsigned*)(Ow + (size_t)orow * ldo + d0 * 32 + r32) = cvt4_fp8(v, v1, v2, v3); } }
.LBB0_1452:
	s_or_b64 exec, exec, s[42:43]
	v_mov_b32_e32 v2, v240
	v_rcp_f32_e32 v2, v2
	s_nop 0
	v_mul_f32_e32 v2, 0x41800000, v2
	v_mul_f32_e32 v3, v41, v2
	s_nop 1
	v_mov_b32_dpp v5, v3 quad_perm:[1,0,3,2] row_mask:0xf bank_mask:0xf
	s_nop 1
	v_mov_b32_dpp v4, v3 quad_perm:[2,3,0,1] row_mask:0xf bank_mask:0xf
	s_waitcnt lgkmcnt(0)
	s_nop 1
	v_mov_b32_dpp v6, v5 quad_perm:[2,3,0,1] row_mask:0xf bank_mask:0xf
	s_and_saveexec_b64 s[42:43], s[6:7]
	s_cbranch_execz .LBB0_1454
	v_mov_b32_e32 v7, v147
	v_cvt_pk_fp8_f32 v7, v3, v5
	s_waitcnt lgkmcnt(0)
	v_cvt_pk_fp8_f32 v7, v4, v6 op_sel:[0,0,1]
	v_add_co_u32_e32 v4, vcc, 0x5000, v66
	s_nop 1
	v_addc_co_u32_e32 v5, vcc, 0, v67, vcc
	global_store_dword v[4:5], v7, off offset:2048

; __device__ __forceinline__ unsigned cvt4_fp8(float a, float b, float c, float d) { int w = 0; w = __builtin_amdgcn_cvt_pk_fp8_f32(a, b, w, false); w = __builtin_amdgcn_cvt_pk_fp8_f32(c, d, w, true); return (unsigned)w; }
; template <bool MLA>
; __device__ __forceinline__ void attn_unit(char* lds, int h, int qb, const bf16_t* Qp, int ldq, const bf16_t* Kp, int ldk, const bf16_t* KRp, const bf16_t* Vp, int ldv,
;                                           unsigned char* Op, int ldo, const float* KMp, const float* rel_bias) {
;     ...
;     for (int r = 0; r < 16; ++r) { const int orow = CROWC(r) + 4 * hi; const float rl = 16.0f * __builtin_amdgcn_rcpf(li_h[CROWC(r)]);
; #pragma unroll
;         for (int d0 = 0; d0 < 4; ++d0) { const float v = o[d0][r] * rl; const float v1 = __shfl_xor(v, 1), v2 = __shfl_xor(v, 2), v3 = __shfl_xor(v1, 2);
;             if ((r32 & 3) == 0) *(unsigned*)(Ow + (size_t)orow * ldo + d0 * 32 + r32) = cvt4_fp8(v, v1, v2, v3); } }
.LBB0_1460:
	s_or_b64 exec, exec, s[42:43]
	v_mov_b32_e32 v2, v241
	v_rcp_f32_e32 v2, v2
	s_nop 0
	v_mul_f32_e32 v2, 0x41800000, v2
	v_mul_f32_e32 v3, v42, v2
	s_nop 1
	v_mov_b32_dpp v5, v3 quad_perm:[1,0,3,2] row_mask:0xf bank_mask:0xf
	s_nop 1
	v_mov_b32_dpp v4, v3 quad_perm:[2,3,0,1] row_mask:0xf bank_mask:0xf
	s_waitcnt lgkmcnt(0)
	s_nop 1
	v_mov_b32_dpp v6, v5 quad_perm:[2,3,0,1] row_mask:0xf bank_mask:0xf
	s_and_saveexec_b64 s[42:43], s[6:7]
	s_cbranch_execz .LBB0_1462
	v_mov_b32_e32 v7, v147
	v_cvt_pk_fp8_f32 v7, v3, v5
	s_waitcnt lgkmcnt(0)
	v_cvt_pk_fp8_f32 v7, v4, v6 op_sel:[0,0,1]
	v_add_co_u32_e32 v4, vcc, 0x8000, v66
	s_nop 1
	v_addc_co_u32_e32 v5, vcc, 0, v67, vcc
	global_store_dword v[4:5], v7, off

; __device__ __forceinline__ unsigned cvt4_fp8(float a, float b, float c, float d) { int w = 0; w = __builtin_amdgcn_cvt_pk_fp8_f32(a, b, w, false); w = __builtin_amdgcn_cvt_pk_fp8_f32(c, d, w, true); return (unsigned)w; }
; template <bool MLA>
; __device__ __forceinline__ void attn_unit(char* lds, int h, int qb, const bf16_t* Qp, int ldq, const bf16_t* Kp, int ldk, const bf16_t* KRp, const bf16_t* Vp, int ldv,
;                                           unsigned char* Op, int ldo, const float* KMp, const float* rel_bias) {
;     ...
;     for (int r = 0; r < 16; ++r) { const int orow = CROWC(r) + 4 * hi; const float rl = 16.0f * __builtin_amdgcn_rcpf(li_h[CROWC(r)]);
; #pragma unroll
;         for (int d0 = 0; d0 < 4; ++d0) { const float v = o[d0][r] * rl; const float v1 = __shfl_xor(v, 1), v2 = __shfl_xor(v, 2), v3 = __shfl_xor(v1, 2);
;             if ((r32 & 3) == 0) *(unsigned*)(Ow + (size_t)orow * ldo + d0 * 32 + r32) = cvt4_fp8(v, v1, v2, v3); } }
.LBB0_1468:
	s_or_b64 exec, exec, s[42:43]
	v_mov_b32_e32 v2, v242
	v_rcp_f32_e32 v2, v2
	s_nop 0
	v_mul_f32_e32 v2, 0x41800000, v2
	v_mul_f32_e32 v3, v43, v2
	s_nop 1
	v_mov_b32_dpp v5, v3 quad_perm:[1,0,3,2] row_mask:0xf bank_mask:0xf
	s_nop 1
	v_mov_b32_dpp v4, v3 quad_perm:[2,3,0,1] row_mask:0xf bank_mask:0xf
	s_waitcnt lgkmcnt(0)
	s_nop 1
	v_mov_b32_dpp v6, v5 quad_perm:[2,3,0,1] row_mask:0xf bank_mask:0xf
	s_and_saveexec_b64 s[42:43], s[6:7]
	s_cbranch_execz .LBB0_1470
	v_mov_b32_e32 v7, v147
	v_cvt_pk_fp8_f32 v7, v3, v5
	s_waitcnt lgkmcnt(0)
	v_cvt_pk_fp8_f32 v7, v4, v6 op_sel:[0,0,1]
	v_add_co_u32_e32 v4, vcc, 0x8000, v66
	s_nop 1
	v_addc_co_u32_e32 v5, vcc, 0, v67, vcc
	global_store_dword v[4:5], v7, off offset:2048

; __device__ __forceinline__ unsigned cvt4_fp8(float a, float b, float c, float d) { int w = 0; w = __builtin_amdgcn_cvt_pk_fp8_f32(a, b, w, false); w = __builtin_amdgcn_cvt_pk_fp8_f32(c, d, w, true); return (unsigned)w; }
; template <bool MLA>
; __device__ __forceinline__ void attn_unit(char* lds, int h, int qb, const bf16_t* Qp, int ldq, const bf16_t* Kp, int ldk, const bf16_t* KRp, const bf16_t* Vp, int ldv,
;                                           unsigned char* Op, int ldo, const float* KMp, const float* rel_bias) {
;     ...
;     for (int r = 0; r < 16; ++r) { const int orow = CROWC(r) + 4 * hi; const float rl = 16.0f * __builtin_amdgcn_rcpf(li_h[CROWC(r)]);
; #pragma unroll
;         for (int d0 = 0; d0 < 4; ++d0) { const float v = o[d0][r] * rl; const float v1 = __shfl_xor(v, 1), v2 = __shfl_xor(v, 2), v3 = __shfl_xor(v1, 2);
;             if ((r32 & 3) == 0) *(unsigned*)(Ow + (size_t)orow * ldo + d0 * 32 + r32) = cvt4_fp8(v, v1, v2, v3); } }
.LBB0_1476:
	s_or_b64 exec, exec, s[42:43]
	v_mov_b32_e32 v2, v243
	v_rcp_f32_e32 v2, v2
	s_nop 0
	v_mul_f32_e32 v2, 0x41800000, v2
	v_mul_f32_e32 v3, v44, v2
	s_nop 1
	v_mov_b32_dpp v5, v3 quad_perm:[1,0,3,2] row_mask:0xf bank_mask:0xf
	s_nop 1
	v_mov_b32_dpp v4, v3 quad_perm:[2,3,0,1] row_mask:0xf bank_mask:0xf
	s_waitcnt lgkmcnt(0)
	s_nop 1
	v_mov_b32_dpp v6, v5 quad_perm:[2,3,0,1] row_mask:0xf bank_mask:0xf
	s_and_saveexec_b64 s[42:43], s[6:7]
	s_cbranch_execz .LBB0_1478
	v_mov_b32_e32 v7, v147
	v_cvt_pk_fp8_f32 v7, v3, v5
	s_waitcnt lgkmcnt(0)
	v_cvt_pk_fp8_f32 v7, v4, v6 op_sel:[0,0,1]
	v_add_co_u32_e32 v4, vcc, 0x9000, v66
	s_nop 1
	v_addc_co_u32_e32 v5, vcc, 0, v67, vcc
	global_store_dword v[4:5], v7, off

; __device__ __forceinline__ unsigned cvt4_fp8(float a, float b, float c, float d) { int w = 0; w = __builtin_amdgcn_cvt_pk_fp8_f32(a, b, w, false); w = __builtin_amdgcn_cvt_pk_fp8_f32(c, d, w, true); return (unsigned)w; }
; template <bool MLA>
; __device__ __forceinline__ void attn_unit(char* lds, int h, int qb, const bf16_t* Qp, int ldq, const bf16_t* Kp, int ldk, const bf16_t* KRp, const bf16_t* Vp, int ldv,
;                                           unsigned char* Op, int ldo, const float* KMp, const float* rel_bias) {
;     ...
;     for (int r = 0; r < 16; ++r) { const int orow = CROWC(r) + 4 * hi; const float rl = 16.0f * __builtin_amdgcn_rcpf(li_h[CROWC(r)]);
; #pragma unroll
;         for (int d0 = 0; d0 < 4; ++d0) { const float v = o[d0][r] * rl; const float v1 = __shfl_xor(v, 1), v2 = __shfl_xor(v, 2), v3 = __shfl_xor(v1, 2);
;             if ((r32 & 3) == 0) *(unsigned*)(Ow + (size_t)orow * ldo + d0 * 32 + r32) = cvt4_fp8(v, v1, v2, v3); } }
.LBB0_1484:
	s_or_b64 exec, exec, s[42:43]
	v_mov_b32_e32 v2, v244
	v_rcp_f32_e32 v2, v2
	s_nop 0
	v_mul_f32_e32 v2, 0x41800000, v2
	v_mul_f32_e32 v3, v45, v2
	s_nop 1
	v_mov_b32_dpp v5, v3 quad_perm:[1,0,3,2] row_mask:0xf bank_mask:0xf
	s_nop 1
	v_mov_b32_dpp v4, v3 quad_perm:[2,3,0,1] row_mask:0xf bank_mask:0xf
	s_waitcnt lgkmcnt(0)
	s_nop 1
	v_mov_b32_dpp v6, v5 quad_perm:[2,3,0,1] row_mask:0xf bank_mask:0xf
	s_and_saveexec_b64 s[42:43], s[6:7]
	s_cbranch_execz .LBB0_1486
	v_mov_b32_e32 v7, v147
	v_cvt_pk_fp8_f32 v7, v3, v5
	s_waitcnt lgkmcnt(0)
	v_cvt_pk_fp8_f32 v7, v4, v6 op_sel:[0,0,1]
	v_add_co_u32_e32 v4, vcc, 0x9000, v66
	s_nop 1
	v_addc_co_u32_e32 v5, vcc, 0, v67, vcc
	global_store_dword v[4:5], v7, off offset:2048

; __device__ __forceinline__ unsigned cvt4_fp8(float a, float b, float c, float d) { int w = 0; w = __builtin_amdgcn_cvt_pk_fp8_f32(a, b, w, false); w = __builtin_amdgcn_cvt_pk_fp8_f32(c, d, w, true); return (unsigned)w; }
; template <bool MLA>
; __device__ __forceinline__ void attn_unit(char* lds, int h, int qb, const bf16_t* Qp, int ldq, const bf16_t* Kp, int ldk, const bf16_t* KRp, const bf16_t* Vp, int ldv,
;                                           unsigned char* Op, int ldo, const float* KMp, const float* rel_bias) {
;     ...
;     for (int r = 0; r < 16; ++r) { const int orow = CROWC(r) + 4 * hi; const float rl = 16.0f * __builtin_amdgcn_rcpf(li_h[CROWC(r)]);
; #pragma unroll
;         for (int d0 = 0; d0 < 4; ++d0) { const float v = o[d0][r] * rl; const float v1 = __shfl_xor(v, 1), v2 = __shfl_xor(v, 2), v3 = __shfl_xor(v1, 2);
;             if ((r32 & 3) == 0) *(unsigned*)(Ow + (size_t)orow * ldo + d0 * 32 + r32) = cvt4_fp8(v, v1, v2, v3); } }
.LBB0_1492:
	s_or_b64 exec, exec, s[42:43]
	v_mov_b32_e32 v2, v245
	v_rcp_f32_e32 v2, v2
	s_nop 0
	v_mul_f32_e32 v2, 0x41800000, v2
	v_mul_f32_e32 v3, v46, v2
	s_nop 1
	v_mov_b32_dpp v5, v3 quad_perm:[1,0,3,2] row_mask:0xf bank_mask:0xf
	s_nop 1
	v_mov_b32_dpp v4, v3 quad_perm:[2,3,0,1] row_mask:0xf bank_mask:0xf
	s_waitcnt lgkmcnt(0)
	s_nop 1
	v_mov_b32_dpp v6, v5 quad_perm:[2,3,0,1] row_mask:0xf bank_mask:0xf
	s_and_saveexec_b64 s[42:43], s[6:7]
	s_cbranch_execz .LBB0_1494
	v_mov_b32_e32 v7, v147
	v_cvt_pk_fp8_f32 v7, v3, v5
	s_waitcnt lgkmcnt(0)
	v_cvt_pk_fp8_f32 v7, v4, v6 op_sel:[0,0,1]
	v_add_co_u32_e32 v4, vcc, 0xc000, v66
	s_nop 1
	v_addc_co_u32_e32 v5, vcc, 0, v67, vcc
	global_store_dword v[4:5], v7, off

; __device__ __forceinline__ unsigned cvt4_fp8(float a, float b, float c, float d) { int w = 0; w = __builtin_amdgcn_cvt_pk_fp8_f32(a, b, w, false); w = __builtin_amdgcn_cvt_pk_fp8_f32(c, d, w, true); return (unsigned)w; }
; template <bool MLA>
; __device__ __forceinline__ void attn_unit(char* lds, int h, int qb, const bf16_t* Qp, int ldq, const bf16_t* Kp, int ldk, const bf16_t* KRp, const bf16_t* Vp, int ldv,
;                                           unsigned char* Op, int ldo, const float* KMp, const float* rel_bias) {
;     ...
;     for (int r = 0; r < 16; ++r) { const int orow = CROWC(r) + 4 * hi; const float rl = 16.0f * __builtin_amdgcn_rcpf(li_h[CROWC(r)]);
; #pragma unroll
;         for (int d0 = 0; d0 < 4; ++d0) { const float v = o[d0][r] * rl; const float v1 = __shfl_xor(v, 1), v2 = __shfl_xor(v, 2), v3 = __shfl_xor(v1, 2);
;             if ((r32 & 3) == 0) *(unsigned*)(Ow + (size_t)orow * ldo + d0 * 32 + r32) = cvt4_fp8(v, v1, v2, v3); } }
.LBB0_1500:
	s_or_b64 exec, exec, s[42:43]
	v_mov_b32_e32 v2, v246
	v_rcp_f32_e32 v2, v2
	s_nop 0
	v_mul_f32_e32 v2, 0x41800000, v2
	v_mul_f32_e32 v3, v47, v2
	s_nop 1
	v_mov_b32_dpp v5, v3 quad_perm:[1,0,3,2] row_mask:0xf bank_mask:0xf
	s_nop 1
	v_mov_b32_dpp v4, v3 quad_perm:[2,3,0,1] row_mask:0xf bank_mask:0xf
	s_waitcnt lgkmcnt(0)
	s_nop 1
	v_mov_b32_dpp v6, v5 quad_perm:[2,3,0,1] row_mask:0xf bank_mask:0xf
	s_and_saveexec_b64 s[42:43], s[6:7]
	s_cbranch_execz .LBB0_1502
	v_mov_b32_e32 v7, v147
	v_cvt_pk_fp8_f32 v7, v3, v5
	s_waitcnt lgkmcnt(0)
	v_cvt_pk_fp8_f32 v7, v4, v6 op_sel:[0,0,1]
	v_add_co_u32_e32 v4, vcc, 0xc000, v66
	s_nop 1
	v_addc_co_u32_e32 v5, vcc, 0, v67, vcc
	global_store_dword v[4:5], v7, off offset:2048

; __device__ __forceinline__ unsigned cvt4_fp8(float a, float b, float c, float d) { int w = 0; w = __builtin_amdgcn_cvt_pk_fp8_f32(a, b, w, false); w = __builtin_amdgcn_cvt_pk_fp8_f32(c, d, w, true); return (unsigned)w; }
; template <bool MLA>
; __device__ __forceinline__ void attn_unit(char* lds, int h, int qb, const bf16_t* Qp, int ldq, const bf16_t* Kp, int ldk, const bf16_t* KRp, const bf16_t* Vp, int ldv,
;                                           unsigned char* Op, int ldo, const float* KMp, const float* rel_bias) {
;     ...
;     for (int r = 0; r < 16; ++r) { const int orow = CROWC(r) + 4 * hi; const float rl = 16.0f * __builtin_amdgcn_rcpf(li_h[CROWC(r)]);
; #pragma unroll
;         for (int d0 = 0; d0 < 4; ++d0) { const float v = o[d0][r] * rl; const float v1 = __shfl_xor(v, 1), v2 = __shfl_xor(v, 2), v3 = __shfl_xor(v1, 2);
;             if ((r32 & 3) == 0) *(unsigned*)(Ow + (size_t)orow * ldo + d0 * 32 + r32) = cvt4_fp8(v, v1, v2, v3); } }
.LBB0_1508:
	s_or_b64 exec, exec, s[42:43]
	v_mov_b32_e32 v2, v247
	v_rcp_f32_e32 v2, v2
	s_nop 0
	v_mul_f32_e32 v2, 0x41800000, v2
	v_mul_f32_e32 v3, v48, v2
	s_nop 1
	v_mov_b32_dpp v5, v3 quad_perm:[1,0,3,2] row_mask:0xf bank_mask:0xf
	s_nop 1
	v_mov_b32_dpp v4, v3 quad_perm:[2,3,0,1] row_mask:0xf bank_mask:0xf
	s_waitcnt lgkmcnt(0)
	s_nop 1
	v_mov_b32_dpp v6, v5 quad_perm:[2,3,0,1] row_mask:0xf bank_mask:0xf
	s_and_saveexec_b64 s[42:43], s[6:7]
	s_cbranch_execz .LBB0_1510
	v_mov_b32_e32 v7, v147
	v_cvt_pk_fp8_f32 v7, v3, v5
	s_waitcnt lgkmcnt(0)
	v_cvt_pk_fp8_f32 v7, v4, v6 op_sel:[0,0,1]
	v_add_co_u32_e32 v4, vcc, 0xd000, v66
	s_nop 1
	v_addc_co_u32_e32 v5, vcc, 0, v67, vcc
	global_store_dword v[4:5], v7, off

; __device__ __forceinline__ unsigned cvt4_fp8(float a, float b, float c, float d) { int w = 0; w = __builtin_amdgcn_cvt_pk_fp8_f32(a, b, w, false); w = __builtin_amdgcn_cvt_pk_fp8_f32(c, d, w, true); return (unsigned)w; }
; template <bool MLA>
; __device__ __forceinline__ void attn_unit(char* lds, int h, int qb, const bf16_t* Qp, int ldq, const bf16_t* Kp, int ldk, const bf16_t* KRp, const bf16_t* Vp, int ldv,
;                                           unsigned char* Op, int ldo, const float* KMp, const float* rel_bias) {
;     ...
;     for (int r = 0; r < 16; ++r) { const int orow = CROWC(r) + 4 * hi; const float rl = 16.0f * __builtin_amdgcn_rcpf(li_h[CROWC(r)]);
; #pragma unroll
;         for (int d0 = 0; d0 < 4; ++d0) { const float v = o[d0][r] * rl; const float v1 = __shfl_xor(v, 1), v2 = __shfl_xor(v, 2), v3 = __shfl_xor(v1, 2);
;             if ((r32 & 3) == 0) *(unsigned*)(Ow + (size_t)orow * ldo + d0 * 32 + r32) = cvt4_fp8(v, v1, v2, v3); } }
.LBB0_1516:
	s_or_b64 exec, exec, s[42:43]
	v_mov_b32_e32 v2, v248
	v_rcp_f32_e32 v2, v2
	s_nop 0
	v_mul_f32_e32 v2, 0x41800000, v2
	v_mul_f32_e32 v3, v49, v2
	s_nop 1
	v_mov_b32_dpp v5, v3 quad_perm:[1,0,3,2] row_mask:0xf bank_mask:0xf
	s_nop 1
	v_mov_b32_dpp v4, v3 quad_perm:[2,3,0,1] row_mask:0xf bank_mask:0xf
	s_waitcnt lgkmcnt(0)
	s_nop 1
	v_mov_b32_dpp v6, v5 quad_perm:[2,3,0,1] row_mask:0xf bank_mask:0xf
	s_and_saveexec_b64 s[42:43], s[6:7]
	s_cbranch_execz .LBB0_1518
	v_mov_b32_e32 v7, v147
	v_cvt_pk_fp8_f32 v7, v3, v5
	s_waitcnt lgkmcnt(0)
	v_cvt_pk_fp8_f32 v7, v4, v6 op_sel:[0,0,1]
	v_add_co_u32_e32 v4, vcc, 0xd000, v66
	s_nop 1
	v_addc_co_u32_e32 v5, vcc, 0, v67, vcc
	global_store_dword v[4:5], v7, off offset:2048

; template <bool MLA>
; __device__ __forceinline__ void attn_unit(char* lds, int h, int qb, const bf16_t* Qp, int ldq, const bf16_t* Kp, int ldk, const bf16_t* KRp, const bf16_t* Vp, int ldv,
;                                           unsigned char* Op, int ldo, const float* KMp, const float* rel_bias) {
;     ...
;         if (t + 1 < NT) A_ISSUE(kb + 64, buf ^ 1);
;         int act;
;         if (MLA || jb == qb) act = (kb <= qlo + 31) ? 1 : 0; else act = __any((int)((mysel >> jb) & 1u)) ? 1 : 0;
;         act = __builtin_amdgcn_readfirstlane(act);
;         if (act) {
;             f32x16 p0, p1;
; #pragma unroll
;             for (int r = 0; r < 16; ++r) { p0[r] = 0.f; p1[r] = 0.f; }
;             { const char* kn = lds + buf * SHM_KN; const char* kr = lds + buf * SHM_KR;
; #pragma unroll
;               for (int d0 = 0; d0 < 8; ++d0) { const char* ap = kn + kan[d0 & 3] + (d0 >> 2) * 128;
;                   const bf16x8 a0 = *(const bf16x8*)ap, a1 = *(const bf16x8*)(ap + 32 * 256);
;                   p0 = __builtin_amdgcn_mfma_f32_32x32x16_bf16(a0, qr[d0], p0, 0, 0, 0);
;                   p1 = __builtin_amdgcn_mfma_f32_32x32x16_bf16(a1, qr[d0], p1, 0, 0, 0); }
;               if constexpr (MLA) {
; #pragma unroll
;                   for (int d0 = 8; d0 < 12; ++d0) { const char* ap = kr + kar[d0 & 3];
;                       const bf16x8 a0 = *(const bf16x8*)ap, a1 = *(const bf16x8*)(ap + 32 * 128);
;                       p0 = __builtin_amdgcn_mfma_f32_32x32x16_bf16(a0, qr[d0], p0, 0, 0, 0);
;                       p1 = __builtin_amdgcn_mfma_f32_32x32x16_bf16(a1, qr[d0], p1, 0, 0, 0); } } }
;             const int dq = qpos - kb - 4 * hi;
;             if constexpr (MLA) {
;                 if (kb + 63 > qlo) {
; #pragma unroll
;                     for (int r = 0; r < 16; ++r) { const int d0 = dq - CROWC(r); if (d0 < 0) p0[r] = NEG; if (d0 < 32) p1[r] = NEG; } }
;             } else {
;                 const bool selq = (jb == qb) || (((mysel >> jb) & 1u) != 0u);
;                 if (q0 - (kb + 63) >= 128) { const float cb = bt_l[128];
; #pragma unroll
;                     for (int r = 0; r < 16; ++r) { p0[r] = selq ? p0[r] + cb : NEG; p1[r] = selq ? p1[r] + cb : NEG; } }
;                 else {
; #pragma unroll
;                     for (int r4 = 0; r4 < 4; ++r4) {
; #pragma unroll
.LBB0_1559:
	s_bitcmp0_b32 s54, 0
	s_cbranch_scc1 .Lmoba_inact
	s_add_i32 s22, s75, 0
	v_add_u32_e32 v2, s22, v203
	ds_read_b128 v[68:71], v2 offset:32768
	ds_read_b128 v[72:75], v2 offset:32896
	s_mov_b64 s[54:55], -1
	s_waitcnt lgkmcnt(0)
	v_mfma_f32_32x32x16_bf16 v[100:115], v[68:71], v[160:163], 0
	s_xor_b32 s100, s75, 0x4000
	s_add_i32 s100, s27, s100
	v_lshl_add_u64 v[228:229], s[52:53], 0, v[182:183]
	s_add_i32 m0, s100, 0x8000
	s_nop 0
	global_load_lds_dwordx4 v[228:229], off
	ds_read_b128 v[68:71], v2 offset:40960
	ds_read_b128 v[76:79], v2 offset:41088
	v_add_u32_e32 v2, s22, v204
	s_waitcnt lgkmcnt(0)
	v_mfma_f32_32x32x16_bf16 v[84:99], v[68:71], v[160:163], 0
	v_lshl_add_u64 v[228:229], s[52:53], 0, v[180:181]
	v_lshl_add_u64 v[230:231], v[228:229], 0, s[46:47]
	s_mov_b32 m0, s100
	v_lshl_add_u64 v[228:229], v[228:229], 0, s[48:49]
	global_load_lds_dwordx4 v[230:231], off
	ds_read_b128 v[68:71], v2 offset:32768
	ds_read_b128 v[80:83], v2 offset:32896
	s_waitcnt lgkmcnt(0)
	v_mfma_f32_32x32x16_bf16 v[100:115], v[68:71], v[156:159], v[100:115]
	v_lshl_add_u64 v[230:231], s[52:53], 0, v[184:185]
	s_add_i32 m0, s100, 0x8400
	s_nop 0
	global_load_lds_dwordx4 v[230:231], off
	ds_read_b128 v[68:71], v2 offset:40960
	ds_read_b128 v[116:119], v2 offset:41088
	v_add_u32_e32 v2, s22, v205
	s_waitcnt lgkmcnt(0)
	v_mfma_f32_32x32x16_bf16 v[84:99], v[68:71], v[156:159], v[84:99]
	s_add_i32 m0, s100, 0x400
	s_nop 0
	global_load_lds_dwordx4 v[228:229], off
	ds_read_b128 v[68:71], v2 offset:32768
	ds_read_b128 v[120:123], v2 offset:32896
	s_waitcnt lgkmcnt(0)
	v_mfma_f32_32x32x16_bf16 v[100:115], v[68:71], v[152:155], v[100:115]
	ds_read_b128 v[68:71], v2 offset:40960
	ds_read_b128 v[124:127], v2 offset:41088
	v_add_u32_e32 v2, s22, v206
	s_lshl_b32 s22, 1, s76
	s_waitcnt lgkmcnt(0)
	v_mfma_f32_32x32x16_bf16 v[84:99], v[68:71], v[152:155], v[84:99]
	ds_read_b128 v[68:71], v2 offset:32768
	ds_read_b128 v[128:131], v2 offset:32896
	s_waitcnt lgkmcnt(0)
	v_mfma_f32_32x32x16_bf16 v[100:115], v[68:71], v[148:151], v[100:115]
	ds_read_b128 v[68:71], v2 offset:40960
	ds_read_b128 v[222:225], v2 offset:41088
	v_and_b32_e32 v2, s22, v219
	v_cmp_ne_u32_e32 vcc, 0, v2
	s_or_b64 s[12:13], s[12:13], vcc
	s_cmpk_gt_i32 s69, 0x7f
	s_waitcnt lgkmcnt(0)
	v_mfma_f32_32x32x16_bf16 v[84:99], v[68:71], v[148:151], v[84:99]
	v_mfma_f32_32x32x16_bf16 v[100:115], v[72:75], v[144:147], v[100:115]
	v_mfma_f32_32x32x16_bf16 v[84:99], v[76:79], v[144:147], v[84:99]
	v_mfma_f32_32x32x16_bf16 v[100:115], v[80:83], v[140:143], v[100:115]
	v_mfma_f32_32x32x16_bf16 v[84:99], v[116:119], v[140:143], v[84:99]
	v_mfma_f32_32x32x16_bf16 v[100:115], v[120:123], v[136:139], v[100:115]
	v_mfma_f32_32x32x16_bf16 v[84:99], v[124:127], v[136:139], v[84:99]
	v_mfma_f32_32x32x16_bf16 v[100:115], v[128:131], v[132:135], v[100:115]
	v_mfma_f32_32x32x16_bf16 v[84:99], v[222:225], v[132:135], v[84:99]
	s_cbranch_scc1 .LBB0_1594
	v_add_u32_e32 v2, s69, v220
	v_add_u32_e32 v2, 63, v2
	v_min_u32_e32 v222, 0x80, v2
	v_lshl_add_u32 v222, v222, 2, 0
	v_add_u32_e32 v222, 0x14c00, v222
	ds_read_b32 v68, v222
	v_med3_i32 v223, v2, 32, v214
	v_lshl_add_u32 v223, v223, 2, s16
	v_add_u32_e32 v223, 0xffffff80, v223
	ds_read_b32 v116, v223
	v_add_u32_e32 v221, -1, v2
	v_min_u32_e32 v222, 0x80, v221
	v_lshl_add_u32 v222, v222, 2, 0
	v_add_u32_e32 v222, 0x14c00, v222
	ds_read_b32 v69, v222
	v_med3_i32 v223, v221, 32, v214
	v_lshl_add_u32 v223, v223, 2, s16
	v_add_u32_e32 v223, 0xffffff80, v223
	ds_read_b32 v117, v223
	v_add_u32_e32 v221, -2, v2
	v_min_u32_e32 v222, 0x80, v221
	v_lshl_add_u32 v222, v222, 2, 0
	v_add_u32_e32 v222, 0x14c00, v222
	ds_read_b32 v70, v222
	v_med3_i32 v223, v221, 32, v214
	v_lshl_add_u32 v223, v223, 2, s16
	v_add_u32_e32 v223, 0xffffff80, v223
	ds_read_b32 v118, v223
	v_add_u32_e32 v221, -3, v2
	v_min_u32_e32 v222, 0x80, v221
	v_lshl_add_u32 v222, v222, 2, 0
	v_add_u32_e32 v222, 0x14c00, v222
	ds_read_b32 v71, v222
	v_med3_i32 v223, v221, 32, v214
	v_lshl_add_u32 v223, v223, 2, s16
	v_add_u32_e32 v223, 0xffffff80, v223
	ds_read_b32 v119, v223
	v_add_u32_e32 v221, -8, v2
	v_min_u32_e32 v222, 0x80, v221
	v_lshl_add_u32 v222, v222, 2, 0
	v_add_u32_e32 v222, 0x14c00, v222
	ds_read_b32 v72, v222
	v_med3_i32 v223, v221, 32, v214
	v_lshl_add_u32 v223, v223, 2, s16
	v_add_u32_e32 v223, 0xffffff80, v223
	ds_read_b32 v120, v223
	v_add_u32_e32 v221, -9, v2
	v_min_u32_e32 v222, 0x80, v221
	v_lshl_add_u32 v222, v222, 2, 0
	v_add_u32_e32 v222, 0x14c00, v222
	ds_read_b32 v73, v222
	v_med3_i32 v223, v221, 32, v214
	v_lshl_add_u32 v223, v223, 2, s16
	v_add_u32_e32 v223, 0xffffff80, v223
	ds_read_b32 v121, v223
	v_add_u32_e32 v221, -10, v2
	v_min_u32_e32 v222, 0x80, v221
	v_lshl_add_u32 v222, v222, 2, 0
	v_add_u32_e32 v222, 0x14c00, v222
	ds_read_b32 v74, v222
	v_med3_i32 v223, v221, 32, v214
	v_lshl_add_u32 v223, v223, 2, s16
	v_add_u32_e32 v223, 0xffffff80, v223
	ds_read_b32 v122, v223
	v_add_u32_e32 v221, -11, v2
	v_min_u32_e32 v222, 0x80, v221
	v_lshl_add_u32 v222, v222, 2, 0
	v_add_u32_e32 v222, 0x14c00, v222
	ds_read_b32 v75, v222
	v_med3_i32 v223, v221, 32, v214
	v_lshl_add_u32 v223, v223, 2, s16
	v_add_u32_e32 v223, 0xffffff80, v223
	ds_read_b32 v123, v223
	v_add_u32_e32 v221, -16, v2
	v_min_u32_e32 v222, 0x80, v221
	v_lshl_add_u32 v222, v222, 2, 0
	v_add_u32_e32 v222, 0x14c00, v222
	ds_read_b32 v76, v222
	v_med3_i32 v223, v221, 32, v214
	v_lshl_add_u32 v223, v223, 2, s16
	v_add_u32_e32 v223, 0xffffff80, v223
	ds_read_b32 v124, v223
	v_add_u32_e32 v221, 0xffffffef, v2
	v_min_u32_e32 v222, 0x80, v221
	v_lshl_add_u32 v222, v222, 2, 0
	v_add_u32_e32 v222, 0x14c00, v222
	ds_read_b32 v77, v222
; #define SBAR() __builtin_amdgcn_sched_barrier(0)
; template <bool MLA>
; __device__ __forceinline__ void attn_unit(char* lds, int h, int qb, const bf16_t* Qp, int ldq, const bf16_t* Kp, int ldk, const bf16_t* KRp, const bf16_t* Vp, int ldv,
;                                           unsigned char* Op, int ldo, const float* KMp, const float* rel_bias) {
;     ...
;                 else {
; #pragma unroll
;                     for (int r4 = 0; r4 < 4; ++r4) {
; #pragma unroll
;                         for (int rr = 0; rr < 4; ++rr) { const int r = r4 * 4 + rr; const int d0 = dq - CROWC(r), d1 = d0 - 32;
;                             const float b0 = bt_l[d0 < 0 ? 0 : (d0 > 128 ? 128 : d0)], b1 = bt_l[d1 < 0 ? 0 : (d1 > 128 ? 128 : d1)];
;                             p0[r] = (selq && d0 >= 0) ? p0[r] + b0 : NEG; p1[r] = (selq && d1 >= 0) ? p1[r] + b1 : NEG; }
;                         SBAR(); } }
	v_med3_i32 v223, v221, 32, v214
	v_lshl_add_u32 v223, v223, 2, s16
	v_add_u32_e32 v223, 0xffffff80, v223
	ds_read_b32 v125, v223
	v_add_u32_e32 v221, 0xffffffee, v2
	v_min_u32_e32 v222, 0x80, v221
	v_lshl_add_u32 v222, v222, 2, 0
	v_add_u32_e32 v222, 0x14c00, v222
	ds_read_b32 v78, v222
	v_med3_i32 v223, v221, 32, v214
	v_lshl_add_u32 v223, v223, 2, s16
	v_add_u32_e32 v223, 0xffffff80, v223
	ds_read_b32 v126, v223
	v_add_u32_e32 v221, 0xffffffed, v2
	v_min_u32_e32 v222, 0x80, v221
	v_lshl_add_u32 v222, v222, 2, 0
	v_add_u32_e32 v222, 0x14c00, v222
	ds_read_b32 v79, v222
	v_med3_i32 v223, v221, 32, v214
	v_lshl_add_u32 v223, v223, 2, s16
	v_add_u32_e32 v223, 0xffffff80, v223
	ds_read_b32 v127, v223
	v_add_u32_e32 v221, 0xffffffe8, v2
	v_min_u32_e32 v222, 0x80, v221
	v_lshl_add_u32 v222, v222, 2, 0
	v_add_u32_e32 v222, 0x14c00, v222
	ds_read_b32 v80, v222
	v_med3_i32 v223, v221, 32, v214
	v_lshl_add_u32 v223, v223, 2, s16
	v_add_u32_e32 v223, 0xffffff80, v223
	ds_read_b32 v128, v223
	v_add_u32_e32 v221, 0xffffffe7, v2
	v_min_u32_e32 v222, 0x80, v221
	v_lshl_add_u32 v222, v222, 2, 0
	v_add_u32_e32 v222, 0x14c00, v222
	ds_read_b32 v81, v222
	v_med3_i32 v223, v221, 32, v214
	v_lshl_add_u32 v223, v223, 2, s16
	v_add_u32_e32 v223, 0xffffff80, v223
	ds_read_b32 v129, v223
	v_add_u32_e32 v221, 0xffffffe6, v2
	v_min_u32_e32 v222, 0x80, v221
	v_lshl_add_u32 v222, v222, 2, 0
	v_add_u32_e32 v222, 0x14c00, v222
	ds_read_b32 v82, v222
	v_med3_i32 v223, v221, 32, v214
	v_lshl_add_u32 v223, v223, 2, s16
	v_add_u32_e32 v223, 0xffffff80, v223
	ds_read_b32 v130, v223
	v_add_u32_e32 v221, 0xffffffe5, v2
	v_min_u32_e32 v222, 0x80, v221
	v_lshl_add_u32 v222, v222, 2, 0
	v_add_u32_e32 v222, 0x14c00, v222
	ds_read_b32 v83, v222
	v_med3_i32 v223, v221, 32, v214
	v_lshl_add_u32 v223, v223, 2, s16
	v_add_u32_e32 v223, 0xffffff80, v223
	ds_read_b32 v131, v223
	s_waitcnt lgkmcnt(0)
	v_cmp_lt_i32_e32 vcc, -1, v2
	v_add_f32_e32 v68, v100, v68
	s_and_b64 vcc, vcc, s[12:13]
	v_cndmask_b32_e32 v68, v215, v68, vcc
	v_cmp_lt_i32_e32 vcc, 31, v2
	v_add_f32_e32 v116, v84, v116
	s_and_b64 vcc, vcc, s[12:13]
	v_cndmask_b32_e32 v116, v215, v116, vcc
	v_add_u32_e32 v221, -1, v2
	v_cmp_lt_i32_e32 vcc, -1, v221
	v_add_f32_e32 v69, v101, v69
	s_and_b64 vcc, vcc, s[12:13]
	v_cndmask_b32_e32 v69, v215, v69, vcc
	v_cmp_lt_i32_e32 vcc, 31, v221
	v_add_f32_e32 v117, v85, v117
	s_and_b64 vcc, vcc, s[12:13]
	v_cndmask_b32_e32 v117, v215, v117, vcc
	v_add_u32_e32 v221, -2, v2
	v_cmp_lt_i32_e32 vcc, -1, v221
	v_add_f32_e32 v70, v102, v70
	s_and_b64 vcc, vcc, s[12:13]
	v_cndmask_b32_e32 v70, v215, v70, vcc
	v_cmp_lt_i32_e32 vcc, 31, v221
	v_add_f32_e32 v118, v86, v118
	s_and_b64 vcc, vcc, s[12:13]
	v_cndmask_b32_e32 v118, v215, v118, vcc
	v_add_u32_e32 v221, -3, v2
	v_cmp_lt_i32_e32 vcc, -1, v221
	v_add_f32_e32 v71, v103, v71
	s_and_b64 vcc, vcc, s[12:13]
	v_cndmask_b32_e32 v71, v215, v71, vcc
	v_cmp_lt_i32_e32 vcc, 31, v221
	v_add_f32_e32 v119, v87, v119
	s_and_b64 vcc, vcc, s[12:13]
	v_cndmask_b32_e32 v119, v215, v119, vcc
	v_add_u32_e32 v221, -8, v2
	v_cmp_lt_i32_e32 vcc, -1, v221
	v_add_f32_e32 v72, v104, v72
	s_and_b64 vcc, vcc, s[12:13]
	v_cndmask_b32_e32 v72, v215, v72, vcc
	v_cmp_lt_i32_e32 vcc, 31, v221
	v_add_f32_e32 v120, v88, v120
	s_and_b64 vcc, vcc, s[12:13]
	v_cndmask_b32_e32 v120, v215, v120, vcc
	v_add_u32_e32 v221, -9, v2
	v_cmp_lt_i32_e32 vcc, -1, v221
	v_add_f32_e32 v73, v105, v73
	s_and_b64 vcc, vcc, s[12:13]
	v_cndmask_b32_e32 v73, v215, v73, vcc
	v_cmp_lt_i32_e32 vcc, 31, v221
	v_add_f32_e32 v121, v89, v121
	s_and_b64 vcc, vcc, s[12:13]
	v_cndmask_b32_e32 v121, v215, v121, vcc
	v_add_u32_e32 v221, -10, v2
	v_cmp_lt_i32_e32 vcc, -1, v221
	v_add_f32_e32 v74, v106, v74
	s_and_b64 vcc, vcc, s[12:13]
	v_cndmask_b32_e32 v74, v215, v74, vcc
	v_cmp_lt_i32_e32 vcc, 31, v221
	v_add_f32_e32 v122, v90, v122
	s_and_b64 vcc, vcc, s[12:13]
	v_cndmask_b32_e32 v122, v215, v122, vcc
	v_add_u32_e32 v221, -11, v2
	v_cmp_lt_i32_e32 vcc, -1, v221
	v_add_f32_e32 v75, v107, v75
	s_and_b64 vcc, vcc, s[12:13]
	v_cndmask_b32_e32 v75, v215, v75, vcc
	v_cmp_lt_i32_e32 vcc, 31, v221
	v_add_f32_e32 v123, v91, v123
	s_and_b64 vcc, vcc, s[12:13]
	v_cndmask_b32_e32 v123, v215, v123, vcc
	v_add_u32_e32 v221, -16, v2
	v_cmp_lt_i32_e32 vcc, -1, v221
	v_add_f32_e32 v76, v108, v76
	s_and_b64 vcc, vcc, s[12:13]
	v_cndmask_b32_e32 v76, v215, v76, vcc
	v_cmp_lt_i32_e32 vcc, 31, v221
	v_add_f32_e32 v124, v92, v124
	s_and_b64 vcc, vcc, s[12:13]
	v_cndmask_b32_e32 v124, v215, v124, vcc
	v_add_u32_e32 v221, 0xffffffef, v2
	v_cmp_lt_i32_e32 vcc, -1, v221
	v_add_f32_e32 v77, v109, v77
	s_and_b64 vcc, vcc, s[12:13]
	v_cndmask_b32_e32 v77, v215, v77, vcc
	v_cmp_lt_i32_e32 vcc, 31, v221
	v_add_f32_e32 v125, v93, v125
	s_and_b64 vcc, vcc, s[12:13]
	v_cndmask_b32_e32 v125, v215, v125, vcc
	v_add_u32_e32 v221, 0xffffffee, v2
	v_cmp_lt_i32_e32 vcc, -1, v221
	v_add_f32_e32 v78, v110, v78
	s_and_b64 vcc, vcc, s[12:13]
	v_cndmask_b32_e32 v78, v215, v78, vcc
	v_cmp_lt_i32_e32 vcc, 31, v221
	v_add_f32_e32 v126, v94, v126
	s_and_b64 vcc, vcc, s[12:13]
	v_cndmask_b32_e32 v126, v215, v126, vcc
	v_add_u32_e32 v221, 0xffffffed, v2
	v_cmp_lt_i32_e32 vcc, -1, v221
	v_add_f32_e32 v79, v111, v79
	s_and_b64 vcc, vcc, s[12:13]
	v_cndmask_b32_e32 v79, v215, v79, vcc
	v_cmp_lt_i32_e32 vcc, 31, v221
	v_add_f32_e32 v127, v95, v127
	s_and_b64 vcc, vcc, s[12:13]
	v_cndmask_b32_e32 v127, v215, v127, vcc
	v_add_u32_e32 v221, 0xffffffe8, v2
	v_cmp_lt_i32_e32 vcc, -1, v221
	v_add_f32_e32 v80, v112, v80
	s_and_b64 vcc, vcc, s[12:13]
	v_cndmask_b32_e32 v80, v215, v80, vcc
	v_cmp_lt_i32_e32 vcc, 31, v221
	v_add_f32_e32 v128, v96, v128
	s_and_b64 vcc, vcc, s[12:13]
	v_cndmask_b32_e32 v128, v215, v128, vcc
	v_add_u32_e32 v221, 0xffffffe7, v2
	v_cmp_lt_i32_e32 vcc, -1, v221
	v_add_f32_e32 v81, v113, v81
	s_and_b64 vcc, vcc, s[12:13]
	v_cndmask_b32_e32 v81, v215, v81, vcc
	v_cmp_lt_i32_e32 vcc, 31, v221
	v_add_f32_e32 v129, v97, v129
	s_and_b64 vcc, vcc, s[12:13]
	v_cndmask_b32_e32 v129, v215, v129, vcc
	v_add_u32_e32 v221, 0xffffffe6, v2
	v_cmp_lt_i32_e32 vcc, -1, v221
	v_add_f32_e32 v82, v114, v82
	s_and_b64 vcc, vcc, s[12:13]
	v_cndmask_b32_e32 v82, v215, v82, vcc
	v_cmp_lt_i32_e32 vcc, 31, v221
	v_add_f32_e32 v130, v98, v130
	s_and_b64 vcc, vcc, s[12:13]
	v_cndmask_b32_e32 v130, v215, v130, vcc
	v_add_u32_e32 v221, 0xffffffe5, v2
	v_cmp_lt_i32_e32 vcc, -1, v221
	v_add_f32_e32 v83, v115, v83
	s_and_b64 vcc, vcc, s[12:13]
	v_cndmask_b32_e32 v83, v215, v83, vcc
	v_cmp_lt_i32_e32 vcc, 31, v221
	v_add_f32_e32 v131, v99, v131
	s_and_b64 vcc, vcc, s[12:13]
	v_cndmask_b32_e32 v131, v215, v131, vcc
	s_mov_b64 s[54:55], 0

; template <bool MLA>
; __device__ __forceinline__ void attn_unit(char* lds, int h, int qb, const bf16_t* Qp, int ldq, const bf16_t* Kp, int ldk, const bf16_t* KRp, const bf16_t* Vp, int ldv,
;                                           unsigned char* Op, int ldo, const float* KMp, const float* rel_bias) {
;     ...
;             { const char* kn = lds + buf * SHM_KN; const char* kr = lds + buf * SHM_KR;
; #pragma unroll
;               for (int d0 = 0; d0 < 8; ++d0) { const char* ap = kn + kan[d0 & 3] + (d0 >> 2) * 128;
;                   const bf16x8 a0 = *(const bf16x8*)ap, a1 = *(const bf16x8*)(ap + 32 * 256);
;                   p0 = __builtin_amdgcn_mfma_f32_32x32x16_bf16(a0, qr[d0], p0, 0, 0, 0);
;                   p1 = __builtin_amdgcn_mfma_f32_32x32x16_bf16(a1, qr[d0], p1, 0, 0, 0); }
;               if constexpr (MLA) {
; #pragma unroll
;                   for (int d0 = 8; d0 < 12; ++d0) { const char* ap = kr + kar[d0 & 3];
;                       const bf16x8 a0 = *(const bf16x8*)ap, a1 = *(const bf16x8*)(ap + 32 * 128);
;                       p0 = __builtin_amdgcn_mfma_f32_32x32x16_bf16(a0, qr[d0], p0, 0, 0, 0);
;                       p1 = __builtin_amdgcn_mfma_f32_32x32x16_bf16(a1, qr[d0], p1, 0, 0, 0); } } }
;             const int dq = qpos - kb - 4 * hi;
;             if constexpr (MLA) {
;                 if (kb + 63 > qlo) {
; #pragma unroll
;                     for (int r = 0; r < 16; ++r) { const int d0 = dq - CROWC(r); if (d0 < 0) p0[r] = NEG; if (d0 < 32) p1[r] = NEG; } }
;             } else {
;                 const bool selq = (jb == qb) || (((mysel >> jb) & 1u) != 0u);
;                 if (q0 - (kb + 63) >= 128) { const float cb = bt_l[128];
; #pragma unroll
;                     for (int r = 0; r < 16; ++r) { p0[r] = selq ? p0[r] + cb : NEG; p1[r] = selq ? p1[r] + cb : NEG; } }
;                 else {
; #pragma unroll
;                     for (int r4 = 0; r4 < 4; ++r4) {
; #pragma unroll
;                         for (int rr = 0; rr < 4; ++rr) { const int r = r4 * 4 + rr; const int d0 = dq - CROWC(r), d1 = d0 - 32;
;                             const float b0 = bt_l[d0 < 0 ? 0 : (d0 > 128 ? 128 : d0)], b1 = bt_l[d1 < 0 ? 0 : (d1 > 128 ? 128 : d1)];
;                             p0[r] = (selq && d0 >= 0) ? p0[r] + b0 : NEG; p1[r] = (selq && d1 >= 0) ? p1[r] + b1 : NEG; }
;                         SBAR(); } }
.LBB0_1603:
	s_bitcmp0_b32 s52, 0
	s_cbranch_scc1 .LBB0_1645
	s_lshl_b32 s22, s66, 14
	s_and_b32 s26, s22, 0x4000
	s_add_i32 s22, s26, 0
	v_add_u32_e32 v2, s22, v203
	ds_read_b128 v[68:71], v2 offset:32768
	ds_read_b128 v[72:75], v2 offset:32896
	s_mov_b64 s[52:53], -1
	s_waitcnt lgkmcnt(1)
	v_mfma_f32_32x32x16_bf16 v[100:115], v[68:71], v[160:163], 0
	ds_read_b128 v[68:71], v2 offset:40960
	ds_read_b128 v[76:79], v2 offset:41088
	v_add_u32_e32 v2, s22, v204
	s_waitcnt lgkmcnt(1)
	v_mfma_f32_32x32x16_bf16 v[84:99], v[68:71], v[160:163], 0
	ds_read_b128 v[68:71], v2 offset:32768
	ds_read_b128 v[80:83], v2 offset:32896
	s_waitcnt lgkmcnt(1)
	v_mfma_f32_32x32x16_bf16 v[100:115], v[68:71], v[156:159], v[100:115]
	ds_read_b128 v[68:71], v2 offset:40960
	ds_read_b128 v[116:119], v2 offset:41088
	v_add_u32_e32 v2, s22, v205
	s_waitcnt lgkmcnt(1)
	v_mfma_f32_32x32x16_bf16 v[84:99], v[68:71], v[156:159], v[84:99]
	ds_read_b128 v[68:71], v2 offset:32768
	ds_read_b128 v[120:123], v2 offset:32896
	s_waitcnt lgkmcnt(1)
	v_mfma_f32_32x32x16_bf16 v[100:115], v[68:71], v[152:155], v[100:115]
	ds_read_b128 v[68:71], v2 offset:40960
	ds_read_b128 v[124:127], v2 offset:41088
	v_add_u32_e32 v2, s22, v206
	s_lshl_b32 s22, 1, s27
	s_waitcnt lgkmcnt(1)
	v_mfma_f32_32x32x16_bf16 v[84:99], v[68:71], v[152:155], v[84:99]
	ds_read_b128 v[68:71], v2 offset:32768
	ds_read_b128 v[128:131], v2 offset:32896
	s_waitcnt lgkmcnt(1)
	v_mfma_f32_32x32x16_bf16 v[100:115], v[68:71], v[148:151], v[100:115]
	ds_read_b128 v[68:71], v2 offset:40960
	ds_read_b128 v[152:155], v2 offset:41088
	v_and_b32_e32 v2, s22, v219
	v_cmp_ne_u32_e32 vcc, 0, v2
	s_or_b64 s[12:13], s[12:13], vcc
	s_sub_i32 s22, s65, s54
	s_cmpk_gt_i32 s22, 0x7f
	s_waitcnt lgkmcnt(1)
	v_mfma_f32_32x32x16_bf16 v[84:99], v[68:71], v[148:151], v[84:99]
	v_mfma_f32_32x32x16_bf16 v[100:115], v[72:75], v[144:147], v[100:115]
	v_mfma_f32_32x32x16_bf16 v[84:99], v[76:79], v[144:147], v[84:99]
	v_mfma_f32_32x32x16_bf16 v[100:115], v[80:83], v[140:143], v[100:115]
	v_mfma_f32_32x32x16_bf16 v[84:99], v[116:119], v[140:143], v[84:99]
	v_mfma_f32_32x32x16_bf16 v[100:115], v[120:123], v[136:139], v[100:115]
	v_mfma_f32_32x32x16_bf16 v[84:99], v[124:127], v[136:139], v[84:99]
	v_mfma_f32_32x32x16_bf16 v[100:115], v[128:131], v[132:135], v[100:115]
	s_waitcnt lgkmcnt(0)
	v_mfma_f32_32x32x16_bf16 v[84:99], v[152:155], v[132:135], v[84:99]
	s_cbranch_scc1 .LBB0_1638
	v_subrev_u32_e32 v2, s54, v218
	v_sub_u32_e32 v2, v2, v165
	v_min_u32_e32 v133, 0x80, v2
	v_lshl_add_u32 v133, v133, 2, 0
	v_add_u32_e32 v133, 0x14c00, v133
	ds_read_b32 v68, v133
	v_med3_i32 v134, v2, 32, v214
	v_lshl_add_u32 v134, v134, 2, s16
	v_add_u32_e32 v134, 0xffffff80, v134
	ds_read_b32 v116, v134
	v_add_u32_e32 v132, -1, v2
	v_min_u32_e32 v133, 0x80, v132
	v_lshl_add_u32 v133, v133, 2, 0
	v_add_u32_e32 v133, 0x14c00, v133
	ds_read_b32 v69, v133
	v_med3_i32 v134, v132, 32, v214
	v_lshl_add_u32 v134, v134, 2, s16
	v_add_u32_e32 v134, 0xffffff80, v134
	ds_read_b32 v117, v134
	v_add_u32_e32 v132, -2, v2
	v_min_u32_e32 v133, 0x80, v132
	v_lshl_add_u32 v133, v133, 2, 0
	v_add_u32_e32 v133, 0x14c00, v133
	ds_read_b32 v70, v133
	v_med3_i32 v134, v132, 32, v214
	v_lshl_add_u32 v134, v134, 2, s16
	v_add_u32_e32 v134, 0xffffff80, v134
	ds_read_b32 v118, v134
	v_add_u32_e32 v132, -3, v2
	v_min_u32_e32 v133, 0x80, v132
	v_lshl_add_u32 v133, v133, 2, 0
	v_add_u32_e32 v133, 0x14c00, v133
	ds_read_b32 v71, v133
	v_med3_i32 v134, v132, 32, v214
	v_lshl_add_u32 v134, v134, 2, s16
	v_add_u32_e32 v134, 0xffffff80, v134
	ds_read_b32 v119, v134
	v_add_u32_e32 v132, -8, v2
	v_min_u32_e32 v133, 0x80, v132
	v_lshl_add_u32 v133, v133, 2, 0
	v_add_u32_e32 v133, 0x14c00, v133
	ds_read_b32 v72, v133
	v_med3_i32 v134, v132, 32, v214
	v_lshl_add_u32 v134, v134, 2, s16
	v_add_u32_e32 v134, 0xffffff80, v134
	ds_read_b32 v120, v134
	v_add_u32_e32 v132, -9, v2
	v_min_u32_e32 v133, 0x80, v132
	v_lshl_add_u32 v133, v133, 2, 0
	v_add_u32_e32 v133, 0x14c00, v133
	ds_read_b32 v73, v133
	v_med3_i32 v134, v132, 32, v214
	v_lshl_add_u32 v134, v134, 2, s16
	v_add_u32_e32 v134, 0xffffff80, v134
	ds_read_b32 v121, v134
	v_add_u32_e32 v132, -10, v2
	v_min_u32_e32 v133, 0x80, v132
	v_lshl_add_u32 v133, v133, 2, 0
	v_add_u32_e32 v133, 0x14c00, v133
	ds_read_b32 v74, v133
	v_med3_i32 v134, v132, 32, v214
	v_lshl_add_u32 v134, v134, 2, s16
	v_add_u32_e32 v134, 0xffffff80, v134
	ds_read_b32 v122, v134
	v_add_u32_e32 v132, -11, v2
	v_min_u32_e32 v133, 0x80, v132
	v_lshl_add_u32 v133, v133, 2, 0
	v_add_u32_e32 v133, 0x14c00, v133
	ds_read_b32 v75, v133
	v_med3_i32 v134, v132, 32, v214
	v_lshl_add_u32 v134, v134, 2, s16
	v_add_u32_e32 v134, 0xffffff80, v134
	ds_read_b32 v123, v134
	v_add_u32_e32 v132, -16, v2
	v_min_u32_e32 v133, 0x80, v132
	v_lshl_add_u32 v133, v133, 2, 0
	v_add_u32_e32 v133, 0x14c00, v133
	ds_read_b32 v76, v133
	v_med3_i32 v134, v132, 32, v214
	v_lshl_add_u32 v134, v134, 2, s16
	v_add_u32_e32 v134, 0xffffff80, v134
	ds_read_b32 v124, v134
	v_add_u32_e32 v132, 0xffffffef, v2
	v_min_u32_e32 v133, 0x80, v132
	v_lshl_add_u32 v133, v133, 2, 0
	v_add_u32_e32 v133, 0x14c00, v133
	ds_read_b32 v77, v133
	v_med3_i32 v134, v132, 32, v214
	v_lshl_add_u32 v134, v134, 2, s16
	v_add_u32_e32 v134, 0xffffff80, v134
	ds_read_b32 v125, v134
	v_add_u32_e32 v132, 0xffffffee, v2
	v_min_u32_e32 v133, 0x80, v132
	v_lshl_add_u32 v133, v133, 2, 0
	v_add_u32_e32 v133, 0x14c00, v133
	ds_read_b32 v78, v133
	v_med3_i32 v134, v132, 32, v214
	v_lshl_add_u32 v134, v134, 2, s16
	v_add_u32_e32 v134, 0xffffff80, v134
	ds_read_b32 v126, v134
	v_add_u32_e32 v132, 0xffffffed, v2
	v_min_u32_e32 v133, 0x80, v132
	v_lshl_add_u32 v133, v133, 2, 0
	v_add_u32_e32 v133, 0x14c00, v133
	ds_read_b32 v79, v133
	v_med3_i32 v134, v132, 32, v214
	v_lshl_add_u32 v134, v134, 2, s16
	v_add_u32_e32 v134, 0xffffff80, v134
	ds_read_b32 v127, v134
	v_add_u32_e32 v132, 0xffffffe8, v2
	v_min_u32_e32 v133, 0x80, v132
	v_lshl_add_u32 v133, v133, 2, 0
	v_add_u32_e32 v133, 0x14c00, v133
	ds_read_b32 v80, v133
	v_med3_i32 v134, v132, 32, v214
	v_lshl_add_u32 v134, v134, 2, s16
	v_add_u32_e32 v134, 0xffffff80, v134
	ds_read_b32 v128, v134
	v_add_u32_e32 v132, 0xffffffe7, v2
	v_min_u32_e32 v133, 0x80, v132
	v_lshl_add_u32 v133, v133, 2, 0
	v_add_u32_e32 v133, 0x14c00, v133
	ds_read_b32 v81, v133
	v_med3_i32 v134, v132, 32, v214
	v_lshl_add_u32 v134, v134, 2, s16
	v_add_u32_e32 v134, 0xffffff80, v134
	ds_read_b32 v129, v134
	v_add_u32_e32 v132, 0xffffffe6, v2
	v_min_u32_e32 v133, 0x80, v132
	v_lshl_add_u32 v133, v133, 2, 0
	v_add_u32_e32 v133, 0x14c00, v133
	ds_read_b32 v82, v133
	v_med3_i32 v134, v132, 32, v214
	v_lshl_add_u32 v134, v134, 2, s16
	v_add_u32_e32 v134, 0xffffff80, v134
	ds_read_b32 v130, v134
	v_add_u32_e32 v132, 0xffffffe5, v2
	v_min_u32_e32 v133, 0x80, v132
	v_lshl_add_u32 v133, v133, 2, 0
	v_add_u32_e32 v133, 0x14c00, v133
	ds_read_b32 v83, v133
	v_med3_i32 v134, v132, 32, v214
	v_lshl_add_u32 v134, v134, 2, s16
	v_add_u32_e32 v134, 0xffffff80, v134
	ds_read_b32 v131, v134
	s_waitcnt lgkmcnt(0)
; #define SBAR() __builtin_amdgcn_sched_barrier(0)
; template <bool MLA>
; __device__ __forceinline__ void attn_unit(char* lds, int h, int qb, const bf16_t* Qp, int ldq, const bf16_t* Kp, int ldk, const bf16_t* KRp, const bf16_t* Vp, int ldv,
;                                           unsigned char* Op, int ldo, const float* KMp, const float* rel_bias) {
;     ...
;                 else {
; #pragma unroll
;                     for (int r4 = 0; r4 < 4; ++r4) {
; #pragma unroll
;                         for (int rr = 0; rr < 4; ++rr) { const int r = r4 * 4 + rr; const int d0 = dq - CROWC(r), d1 = d0 - 32;
;                             const float b0 = bt_l[d0 < 0 ? 0 : (d0 > 128 ? 128 : d0)], b1 = bt_l[d1 < 0 ? 0 : (d1 > 128 ? 128 : d1)];
;                             p0[r] = (selq && d0 >= 0) ? p0[r] + b0 : NEG; p1[r] = (selq && d1 >= 0) ? p1[r] + b1 : NEG; }
;                         SBAR(); } }
	v_cmp_lt_i32_e32 vcc, -1, v2
	v_add_f32_e32 v68, v100, v68
	s_and_b64 vcc, vcc, s[12:13]
	v_cndmask_b32_e32 v68, v215, v68, vcc
	v_cmp_lt_i32_e32 vcc, 31, v2
	v_add_f32_e32 v116, v84, v116
	s_and_b64 vcc, vcc, s[12:13]
	v_cndmask_b32_e32 v116, v215, v116, vcc
	v_add_u32_e32 v132, -1, v2
	v_cmp_lt_i32_e32 vcc, -1, v132
	v_add_f32_e32 v69, v101, v69
	s_and_b64 vcc, vcc, s[12:13]
	v_cndmask_b32_e32 v69, v215, v69, vcc
	v_cmp_lt_i32_e32 vcc, 31, v132
	v_add_f32_e32 v117, v85, v117
	s_and_b64 vcc, vcc, s[12:13]
	v_cndmask_b32_e32 v117, v215, v117, vcc
	v_add_u32_e32 v132, -2, v2
	v_cmp_lt_i32_e32 vcc, -1, v132
	v_add_f32_e32 v70, v102, v70
	s_and_b64 vcc, vcc, s[12:13]
	v_cndmask_b32_e32 v70, v215, v70, vcc
	v_cmp_lt_i32_e32 vcc, 31, v132
	v_add_f32_e32 v118, v86, v118
	s_and_b64 vcc, vcc, s[12:13]
	v_cndmask_b32_e32 v118, v215, v118, vcc
	v_add_u32_e32 v132, -3, v2
	v_cmp_lt_i32_e32 vcc, -1, v132
	v_add_f32_e32 v71, v103, v71
	s_and_b64 vcc, vcc, s[12:13]
	v_cndmask_b32_e32 v71, v215, v71, vcc
	v_cmp_lt_i32_e32 vcc, 31, v132
	v_add_f32_e32 v119, v87, v119
	s_and_b64 vcc, vcc, s[12:13]
	v_cndmask_b32_e32 v119, v215, v119, vcc
	v_add_u32_e32 v132, -8, v2
	v_cmp_lt_i32_e32 vcc, -1, v132
	v_add_f32_e32 v72, v104, v72
	s_and_b64 vcc, vcc, s[12:13]
	v_cndmask_b32_e32 v72, v215, v72, vcc
	v_cmp_lt_i32_e32 vcc, 31, v132
	v_add_f32_e32 v120, v88, v120
	s_and_b64 vcc, vcc, s[12:13]
	v_cndmask_b32_e32 v120, v215, v120, vcc
	v_add_u32_e32 v132, -9, v2
	v_cmp_lt_i32_e32 vcc, -1, v132
	v_add_f32_e32 v73, v105, v73
	s_and_b64 vcc, vcc, s[12:13]
	v_cndmask_b32_e32 v73, v215, v73, vcc
	v_cmp_lt_i32_e32 vcc, 31, v132
	v_add_f32_e32 v121, v89, v121
	s_and_b64 vcc, vcc, s[12:13]
	v_cndmask_b32_e32 v121, v215, v121, vcc
	v_add_u32_e32 v132, -10, v2
	v_cmp_lt_i32_e32 vcc, -1, v132
	v_add_f32_e32 v74, v106, v74
	s_and_b64 vcc, vcc, s[12:13]
	v_cndmask_b32_e32 v74, v215, v74, vcc
	v_cmp_lt_i32_e32 vcc, 31, v132
	v_add_f32_e32 v122, v90, v122
	s_and_b64 vcc, vcc, s[12:13]
	v_cndmask_b32_e32 v122, v215, v122, vcc
	v_add_u32_e32 v132, -11, v2
	v_cmp_lt_i32_e32 vcc, -1, v132
	v_add_f32_e32 v75, v107, v75
	s_and_b64 vcc, vcc, s[12:13]
	v_cndmask_b32_e32 v75, v215, v75, vcc
	v_cmp_lt_i32_e32 vcc, 31, v132
	v_add_f32_e32 v123, v91, v123
	s_and_b64 vcc, vcc, s[12:13]
	v_cndmask_b32_e32 v123, v215, v123, vcc
	v_add_u32_e32 v132, -16, v2
	v_cmp_lt_i32_e32 vcc, -1, v132
	v_add_f32_e32 v76, v108, v76
	s_and_b64 vcc, vcc, s[12:13]
	v_cndmask_b32_e32 v76, v215, v76, vcc
	v_cmp_lt_i32_e32 vcc, 31, v132
	v_add_f32_e32 v124, v92, v124
	s_and_b64 vcc, vcc, s[12:13]
	v_cndmask_b32_e32 v124, v215, v124, vcc
	v_add_u32_e32 v132, 0xffffffef, v2
	v_cmp_lt_i32_e32 vcc, -1, v132
	v_add_f32_e32 v77, v109, v77
	s_and_b64 vcc, vcc, s[12:13]
	v_cndmask_b32_e32 v77, v215, v77, vcc
	v_cmp_lt_i32_e32 vcc, 31, v132
	v_add_f32_e32 v125, v93, v125
	s_and_b64 vcc, vcc, s[12:13]
	v_cndmask_b32_e32 v125, v215, v125, vcc
	v_add_u32_e32 v132, 0xffffffee, v2
	v_cmp_lt_i32_e32 vcc, -1, v132
	v_add_f32_e32 v78, v110, v78
	s_and_b64 vcc, vcc, s[12:13]
	v_cndmask_b32_e32 v78, v215, v78, vcc
	v_cmp_lt_i32_e32 vcc, 31, v132
	v_add_f32_e32 v126, v94, v126
	s_and_b64 vcc, vcc, s[12:13]
	v_cndmask_b32_e32 v126, v215, v126, vcc
	v_add_u32_e32 v132, 0xffffffed, v2
	v_cmp_lt_i32_e32 vcc, -1, v132
	v_add_f32_e32 v79, v111, v79
	s_and_b64 vcc, vcc, s[12:13]
	v_cndmask_b32_e32 v79, v215, v79, vcc
	v_cmp_lt_i32_e32 vcc, 31, v132
	v_add_f32_e32 v127, v95, v127
	s_and_b64 vcc, vcc, s[12:13]
	v_cndmask_b32_e32 v127, v215, v127, vcc
	v_add_u32_e32 v132, 0xffffffe8, v2
	v_cmp_lt_i32_e32 vcc, -1, v132
	v_add_f32_e32 v80, v112, v80
	s_and_b64 vcc, vcc, s[12:13]
	v_cndmask_b32_e32 v80, v215, v80, vcc
	v_cmp_lt_i32_e32 vcc, 31, v132
	v_add_f32_e32 v128, v96, v128
	s_and_b64 vcc, vcc, s[12:13]
	v_cndmask_b32_e32 v128, v215, v128, vcc
	v_add_u32_e32 v132, 0xffffffe7, v2
	v_cmp_lt_i32_e32 vcc, -1, v132
	v_add_f32_e32 v81, v113, v81
	s_and_b64 vcc, vcc, s[12:13]
	v_cndmask_b32_e32 v81, v215, v81, vcc
	v_cmp_lt_i32_e32 vcc, 31, v132
	v_add_f32_e32 v129, v97, v129
	s_and_b64 vcc, vcc, s[12:13]
	v_cndmask_b32_e32 v129, v215, v129, vcc
	v_add_u32_e32 v132, 0xffffffe6, v2
	v_cmp_lt_i32_e32 vcc, -1, v132
	v_add_f32_e32 v82, v114, v82
	s_and_b64 vcc, vcc, s[12:13]
	v_cndmask_b32_e32 v82, v215, v82, vcc
	v_cmp_lt_i32_e32 vcc, 31, v132
	v_add_f32_e32 v130, v98, v130
	s_and_b64 vcc, vcc, s[12:13]
	v_cndmask_b32_e32 v130, v215, v130, vcc
	v_add_u32_e32 v132, 0xffffffe5, v2
	v_cmp_lt_i32_e32 vcc, -1, v132
	v_add_f32_e32 v83, v115, v83
	s_and_b64 vcc, vcc, s[12:13]
	v_cndmask_b32_e32 v83, v215, v83, vcc
	v_cmp_lt_i32_e32 vcc, 31, v132
	v_add_f32_e32 v131, v99, v131
	s_and_b64 vcc, vcc, s[12:13]
	v_cndmask_b32_e32 v131, v215, v131, vcc
	s_mov_b64 s[52:53], 0

; #define LDS_WAIT() asm volatile("s_waitcnt lgkmcnt(0)" ::: "memory")
; __device__ __forceinline__ unsigned cvt4_fp8(float a, float b, float c, float d) { int w = 0; w = __builtin_amdgcn_cvt_pk_fp8_f32(a, b, w, false); w = __builtin_amdgcn_cvt_pk_fp8_f32(c, d, w, true); return (unsigned)w; }
; template <bool MLA>
; __device__ __forceinline__ void attn_unit(char* lds, int h, int qb, const bf16_t* Qp, int ldq, const bf16_t* Kp, int ldk, const bf16_t* KRp, const bf16_t* Vp, int ldv,
;                                           unsigned char* Op, int ldo, const float* KMp, const float* rel_bias) {
;     ...
;     if (hi == 0) li_l[r32] = l_reg; LDS_WAIT();
;     unsigned char* Ow = Op + (size_t)qlo * ldo;
; #pragma unroll
;     for (int r = 0; r < 16; ++r) { const int orow = CROWC(r) + 4 * hi; const float rl = 16.0f * __builtin_amdgcn_rcpf(li_h[CROWC(r)]);
; #pragma unroll
;         for (int d0 = 0; d0 < 4; ++d0) { const float v = o[d0][r] * rl; const float v1 = __shfl_xor(v, 1), v2 = __shfl_xor(v, 2), v3 = __shfl_xor(v1, 2);
;             if ((r32 & 3) == 0) *(unsigned*)(Ow + (size_t)orow * ldo + d0 * 32 + r32) = cvt4_fp8(v, v1, v2, v3); } }
; __global__ void __launch_bounds__(512, 2) mega_fwd(Args args) {
;     ...
;         for (;;) { if (tid == 0) MISC[12] = atomicAdd(ctl + CW_AQ2, 1u);
;             __syncthreads(); const int it = (int)MISC[12]; __syncthreads();
.LBB0_1645:
	s_waitcnt vmcnt(0)
	s_barrier
	s_mov_b64 s[98:99], exec
	s_and_b64 exec, exec, s[14:15]
	v_mov_b32_e32 v254, 0
	v_mov_b32_e32 v253, 1
	s_nop 0
	global_atomic_add v253, v254, v253, s[38:39] sc0
	s_mov_b64 exec, s[98:99]
	s_and_saveexec_b64 s[12:13], s[4:5]
	ds_write_b32 v177, v216
	s_or_b64 exec, exec, s[12:13]
	s_waitcnt lgkmcnt(0)
	ds_read_b32 v2, v173
	ds_read_b32 v234, v173 offset:4
	ds_read_b32 v235, v173 offset:8
	ds_read_b32 v236, v173 offset:12
	ds_read_b32 v237, v173 offset:32
	ds_read_b32 v238, v173 offset:36
	ds_read_b32 v239, v173 offset:40
	ds_read_b32 v240, v173 offset:44
	ds_read_b32 v241, v173 offset:64
	ds_read_b32 v242, v173 offset:68
	ds_read_b32 v243, v173 offset:72
	ds_read_b32 v244, v173 offset:76
	ds_read_b32 v245, v173 offset:96
	ds_read_b32 v246, v173 offset:100
	ds_read_b32 v247, v173 offset:104
	ds_read_b32 v248, v173 offset:108
	v_and_b32_e32 v69, 64, v195
	v_xor_b32_e32 v68, 1, v195
	v_add_u32_e32 v69, 64, v69
	v_cmp_lt_i32_e32 vcc, v68, v69
	s_waitcnt lgkmcnt(0)
	v_rcp_f32_e32 v70, v2
	s_lshl_b32 s12, s64, 11
	v_cndmask_b32_e32 v2, v195, v68, vcc
	v_lshlrev_b32_e32 v2, 2, v2
	v_mul_f32_e32 v72, 0x41800000, v70
	v_mul_f32_e32 v73, v52, v72
	s_nop 1
	v_mov_b32_dpp v74, v73 quad_perm:[1,0,3,2] row_mask:0xf bank_mask:0xf
	s_add_u32 s12, s70, s12
	v_xor_b32_e32 v68, 2, v195
	s_addc_u32 s13, s71, 0
	v_cmp_lt_i32_e32 vcc, v68, v69
	s_add_u32 s3, s12, s3
	s_addc_u32 s22, s13, 0
	v_cndmask_b32_e32 v52, v195, v68, vcc
	s_lshl_b64 s[12:13], s[42:43], 11
	v_lshlrev_b32_e32 v52, 2, v52
	s_add_u32 s12, s3, s12
	s_nop 1
	v_mov_b32_dpp v75, v73 quad_perm:[2,3,0,1] row_mask:0xf bank_mask:0xf
	s_waitcnt lgkmcnt(0)
	s_nop 1
	v_mov_b32_dpp v76, v74 quad_perm:[2,3,0,1] row_mask:0xf bank_mask:0xf
	s_addc_u32 s13, s22, s13
	v_lshl_add_u64 v[68:69], s[12:13], 0, v[168:169]
	v_lshl_add_u64 v[70:71], v[68:69], 0, v[170:171]
	v_lshl_add_u64 v[68:69], v[70:71], 0, s[50:51]
	s_and_saveexec_b64 s[12:13], s[6:7]
	s_cbranch_execz .LBB0_1649
	v_mov_b32_e32 v77, v3
	v_cvt_pk_fp8_f32 v77, v73, v74
	s_waitcnt lgkmcnt(0)
	v_cvt_pk_fp8_f32 v77, v75, v76 op_sel:[0,0,1]
	global_store_dword v[68:69], v77, off

; __device__ __forceinline__ unsigned cvt4_fp8(float a, float b, float c, float d) { int w = 0; w = __builtin_amdgcn_cvt_pk_fp8_f32(a, b, w, false); w = __builtin_amdgcn_cvt_pk_fp8_f32(c, d, w, true); return (unsigned)w; }
; template <bool MLA>
; __device__ __forceinline__ void attn_unit(char* lds, int h, int qb, const bf16_t* Qp, int ldq, const bf16_t* Kp, int ldk, const bf16_t* KRp, const bf16_t* Vp, int ldv,
;                                           unsigned char* Op, int ldo, const float* KMp, const float* rel_bias) {
;     ...
;     for (int r = 0; r < 16; ++r) { const int orow = CROWC(r) + 4 * hi; const float rl = 16.0f * __builtin_amdgcn_rcpf(li_h[CROWC(r)]);
; #pragma unroll
;         for (int d0 = 0; d0 < 4; ++d0) { const float v = o[d0][r] * rl; const float v1 = __shfl_xor(v, 1), v2 = __shfl_xor(v, 2), v3 = __shfl_xor(v1, 2);
;             if ((r32 & 3) == 0) *(unsigned*)(Ow + (size_t)orow * ldo + d0 * 32 + r32) = cvt4_fp8(v, v1, v2, v3); } }
.LBB0_1655:
	s_or_b64 exec, exec, s[12:13]
	v_mov_b32_e32 v4, v234
	v_rcp_f32_e32 v4, v4
	s_nop 0
	v_mul_f32_e32 v4, 0x41800000, v4
	v_mul_f32_e32 v20, v53, v4
	s_nop 1
	v_mov_b32_dpp v53, v20 quad_perm:[1,0,3,2] row_mask:0xf bank_mask:0xf
	s_nop 1
	v_mov_b32_dpp v36, v20 quad_perm:[2,3,0,1] row_mask:0xf bank_mask:0xf
	s_waitcnt lgkmcnt(0)
	s_nop 1
	v_mov_b32_dpp v72, v53 quad_perm:[2,3,0,1] row_mask:0xf bank_mask:0xf
	s_and_saveexec_b64 s[12:13], s[6:7]
	s_cbranch_execz .LBB0_1657
	v_mov_b32_e32 v73, v3
	v_cvt_pk_fp8_f32 v73, v20, v53
	s_waitcnt lgkmcnt(0)
	v_cvt_pk_fp8_f32 v73, v36, v72 op_sel:[0,0,1]
	global_store_dword v[70:71], v73, off offset:3072

; __device__ __forceinline__ unsigned cvt4_fp8(float a, float b, float c, float d) { int w = 0; w = __builtin_amdgcn_cvt_pk_fp8_f32(a, b, w, false); w = __builtin_amdgcn_cvt_pk_fp8_f32(c, d, w, true); return (unsigned)w; }
; template <bool MLA>
; __device__ __forceinline__ void attn_unit(char* lds, int h, int qb, const bf16_t* Qp, int ldq, const bf16_t* Kp, int ldk, const bf16_t* KRp, const bf16_t* Vp, int ldv,
;                                           unsigned char* Op, int ldo, const float* KMp, const float* rel_bias) {
;     ...
;     for (int r = 0; r < 16; ++r) { const int orow = CROWC(r) + 4 * hi; const float rl = 16.0f * __builtin_amdgcn_rcpf(li_h[CROWC(r)]);
; #pragma unroll
;         for (int d0 = 0; d0 < 4; ++d0) { const float v = o[d0][r] * rl; const float v1 = __shfl_xor(v, 1), v2 = __shfl_xor(v, 2), v3 = __shfl_xor(v1, 2);
;             if ((r32 & 3) == 0) *(unsigned*)(Ow + (size_t)orow * ldo + d0 * 32 + r32) = cvt4_fp8(v, v1, v2, v3); } }
.LBB0_1663:
	s_or_b64 exec, exec, s[12:13]
	v_mov_b32_e32 v4, v235
	v_rcp_f32_e32 v4, v4
	s_nop 0
	v_mul_f32_e32 v4, 0x41800000, v4
	v_mul_f32_e32 v5, v54, v4
	s_nop 1
	v_mov_b32_dpp v21, v5 quad_perm:[1,0,3,2] row_mask:0xf bank_mask:0xf
	s_nop 1
	v_mov_b32_dpp v20, v5 quad_perm:[2,3,0,1] row_mask:0xf bank_mask:0xf
	s_waitcnt lgkmcnt(0)
	s_nop 1
	v_mov_b32_dpp v36, v21 quad_perm:[2,3,0,1] row_mask:0xf bank_mask:0xf
	s_and_saveexec_b64 s[12:13], s[6:7]
	s_cbranch_execz .LBB0_1665
	v_mov_b32_e32 v37, v3
	v_cvt_pk_fp8_f32 v37, v5, v21
	s_waitcnt lgkmcnt(0)
	v_cvt_pk_fp8_f32 v37, v20, v36 op_sel:[0,0,1]
	v_add_co_u32_e32 v20, vcc, 0x1000, v68
	s_nop 1
	v_addc_co_u32_e32 v21, vcc, 0, v69, vcc
	global_store_dword v[20:21], v37, off

; __device__ __forceinline__ unsigned cvt4_fp8(float a, float b, float c, float d) { int w = 0; w = __builtin_amdgcn_cvt_pk_fp8_f32(a, b, w, false); w = __builtin_amdgcn_cvt_pk_fp8_f32(c, d, w, true); return (unsigned)w; }
; template <bool MLA>
; __device__ __forceinline__ void attn_unit(char* lds, int h, int qb, const bf16_t* Qp, int ldq, const bf16_t* Kp, int ldk, const bf16_t* KRp, const bf16_t* Vp, int ldv,
;                                           unsigned char* Op, int ldo, const float* KMp, const float* rel_bias) {
;     ...
;     for (int r = 0; r < 16; ++r) { const int orow = CROWC(r) + 4 * hi; const float rl = 16.0f * __builtin_amdgcn_rcpf(li_h[CROWC(r)]);
; #pragma unroll
;         for (int d0 = 0; d0 < 4; ++d0) { const float v = o[d0][r] * rl; const float v1 = __shfl_xor(v, 1), v2 = __shfl_xor(v, 2), v3 = __shfl_xor(v1, 2);
;             if ((r32 & 3) == 0) *(unsigned*)(Ow + (size_t)orow * ldo + d0 * 32 + r32) = cvt4_fp8(v, v1, v2, v3); } }
.LBB0_1671:
	s_or_b64 exec, exec, s[12:13]
	v_mov_b32_e32 v4, v236
	v_rcp_f32_e32 v4, v4
	s_nop 0
	v_mul_f32_e32 v4, 0x41800000, v4
	v_mul_f32_e32 v5, v55, v4
	s_nop 1
	v_mov_b32_dpp v20, v5 quad_perm:[1,0,3,2] row_mask:0xf bank_mask:0xf
	s_nop 1
	v_mov_b32_dpp v6, v5 quad_perm:[2,3,0,1] row_mask:0xf bank_mask:0xf
	s_waitcnt lgkmcnt(0)
	s_nop 1
	v_mov_b32_dpp v21, v20 quad_perm:[2,3,0,1] row_mask:0xf bank_mask:0xf
	s_and_saveexec_b64 s[12:13], s[6:7]
	s_cbranch_execz .LBB0_1673
	v_mov_b32_e32 v22, v3
	v_cvt_pk_fp8_f32 v22, v5, v20
	v_add_co_u32_e32 v20, vcc, 0x1000, v68
	s_waitcnt lgkmcnt(0)
	v_cvt_pk_fp8_f32 v22, v6, v21 op_sel:[0,0,1]
	v_addc_co_u32_e32 v21, vcc, 0, v69, vcc
	global_store_dword v[20:21], v22, off offset:2048

; __device__ __forceinline__ unsigned cvt4_fp8(float a, float b, float c, float d) { int w = 0; w = __builtin_amdgcn_cvt_pk_fp8_f32(a, b, w, false); w = __builtin_amdgcn_cvt_pk_fp8_f32(c, d, w, true); return (unsigned)w; }
; template <bool MLA>
; __device__ __forceinline__ void attn_unit(char* lds, int h, int qb, const bf16_t* Qp, int ldq, const bf16_t* Kp, int ldk, const bf16_t* KRp, const bf16_t* Vp, int ldv,
;                                           unsigned char* Op, int ldo, const float* KMp, const float* rel_bias) {
;     ...
;     for (int r = 0; r < 16; ++r) { const int orow = CROWC(r) + 4 * hi; const float rl = 16.0f * __builtin_amdgcn_rcpf(li_h[CROWC(r)]);
; #pragma unroll
;         for (int d0 = 0; d0 < 4; ++d0) { const float v = o[d0][r] * rl; const float v1 = __shfl_xor(v, 1), v2 = __shfl_xor(v, 2), v3 = __shfl_xor(v1, 2);
;             if ((r32 & 3) == 0) *(unsigned*)(Ow + (size_t)orow * ldo + d0 * 32 + r32) = cvt4_fp8(v, v1, v2, v3); } }
.LBB0_1679:
	s_or_b64 exec, exec, s[12:13]
	v_mov_b32_e32 v4, v237
	v_rcp_f32_e32 v4, v4
	s_nop 0
	v_mul_f32_e32 v4, 0x41800000, v4
	v_mul_f32_e32 v5, v56, v4
	s_nop 1
	v_mov_b32_dpp v7, v5 quad_perm:[1,0,3,2] row_mask:0xf bank_mask:0xf
	s_nop 1
	v_mov_b32_dpp v6, v5 quad_perm:[2,3,0,1] row_mask:0xf bank_mask:0xf
	s_waitcnt lgkmcnt(0)
	s_nop 1
	v_mov_b32_dpp v20, v7 quad_perm:[2,3,0,1] row_mask:0xf bank_mask:0xf
	s_and_saveexec_b64 s[12:13], s[6:7]
	s_cbranch_execz .LBB0_1681
	v_mov_b32_e32 v21, v3
	v_cvt_pk_fp8_f32 v21, v5, v7
	s_waitcnt lgkmcnt(0)
	v_cvt_pk_fp8_f32 v21, v6, v20 op_sel:[0,0,1]
	v_add_co_u32_e32 v6, vcc, 0x4000, v68
	s_nop 1
	v_addc_co_u32_e32 v7, vcc, 0, v69, vcc
	global_store_dword v[6:7], v21, off

; __device__ __forceinline__ unsigned cvt4_fp8(float a, float b, float c, float d) { int w = 0; w = __builtin_amdgcn_cvt_pk_fp8_f32(a, b, w, false); w = __builtin_amdgcn_cvt_pk_fp8_f32(c, d, w, true); return (unsigned)w; }
; template <bool MLA>
; __device__ __forceinline__ void attn_unit(char* lds, int h, int qb, const bf16_t* Qp, int ldq, const bf16_t* Kp, int ldk, const bf16_t* KRp, const bf16_t* Vp, int ldv,
;                                           unsigned char* Op, int ldo, const float* KMp, const float* rel_bias) {
;     ...
;     for (int r = 0; r < 16; ++r) { const int orow = CROWC(r) + 4 * hi; const float rl = 16.0f * __builtin_amdgcn_rcpf(li_h[CROWC(r)]);
; #pragma unroll
;         for (int d0 = 0; d0 < 4; ++d0) { const float v = o[d0][r] * rl; const float v1 = __shfl_xor(v, 1), v2 = __shfl_xor(v, 2), v3 = __shfl_xor(v1, 2);
;             if ((r32 & 3) == 0) *(unsigned*)(Ow + (size_t)orow * ldo + d0 * 32 + r32) = cvt4_fp8(v, v1, v2, v3); } }
.LBB0_1687:
	s_or_b64 exec, exec, s[12:13]
	v_mov_b32_e32 v4, v238
	v_rcp_f32_e32 v4, v4
	s_nop 0
	v_mul_f32_e32 v4, 0x41800000, v4
	v_mul_f32_e32 v5, v57, v4
	s_nop 1
	v_mov_b32_dpp v7, v5 quad_perm:[1,0,3,2] row_mask:0xf bank_mask:0xf
	s_nop 1
	v_mov_b32_dpp v6, v5 quad_perm:[2,3,0,1] row_mask:0xf bank_mask:0xf
	s_waitcnt lgkmcnt(0)
	s_nop 1
	v_mov_b32_dpp v8, v7 quad_perm:[2,3,0,1] row_mask:0xf bank_mask:0xf
	s_and_saveexec_b64 s[12:13], s[6:7]
	s_cbranch_execz .LBB0_1689
	v_mov_b32_e32 v20, v3
	v_cvt_pk_fp8_f32 v20, v5, v7
	s_waitcnt lgkmcnt(0)
	v_cvt_pk_fp8_f32 v20, v6, v8 op_sel:[0,0,1]
	v_add_co_u32_e32 v6, vcc, 0x4000, v68
	s_nop 1
	v_addc_co_u32_e32 v7, vcc, 0, v69, vcc
	global_store_dword v[6:7], v20, off offset:2048

; __device__ __forceinline__ unsigned cvt4_fp8(float a, float b, float c, float d) { int w = 0; w = __builtin_amdgcn_cvt_pk_fp8_f32(a, b, w, false); w = __builtin_amdgcn_cvt_pk_fp8_f32(c, d, w, true); return (unsigned)w; }
; template <bool MLA>
; __device__ __forceinline__ void attn_unit(char* lds, int h, int qb, const bf16_t* Qp, int ldq, const bf16_t* Kp, int ldk, const bf16_t* KRp, const bf16_t* Vp, int ldv,
;                                           unsigned char* Op, int ldo, const float* KMp, const float* rel_bias) {
;     ...
;     for (int r = 0; r < 16; ++r) { const int orow = CROWC(r) + 4 * hi; const float rl = 16.0f * __builtin_amdgcn_rcpf(li_h[CROWC(r)]);
; #pragma unroll
;         for (int d0 = 0; d0 < 4; ++d0) { const float v = o[d0][r] * rl; const float v1 = __shfl_xor(v, 1), v2 = __shfl_xor(v, 2), v3 = __shfl_xor(v1, 2);
;             if ((r32 & 3) == 0) *(unsigned*)(Ow + (size_t)orow * ldo + d0 * 32 + r32) = cvt4_fp8(v, v1, v2, v3); } }
.LBB0_1695:
	s_or_b64 exec, exec, s[12:13]
	v_mov_b32_e32 v4, v239
	v_rcp_f32_e32 v4, v4
	s_nop 0
	v_mul_f32_e32 v4, 0x41800000, v4
	v_mul_f32_e32 v5, v58, v4
	s_nop 1
	v_mov_b32_dpp v7, v5 quad_perm:[1,0,3,2] row_mask:0xf bank_mask:0xf
	s_nop 1
	v_mov_b32_dpp v6, v5 quad_perm:[2,3,0,1] row_mask:0xf bank_mask:0xf
	s_waitcnt lgkmcnt(0)
	s_nop 1
	v_mov_b32_dpp v8, v7 quad_perm:[2,3,0,1] row_mask:0xf bank_mask:0xf
	s_and_saveexec_b64 s[12:13], s[6:7]
	s_cbranch_execz .LBB0_1697
	v_mov_b32_e32 v9, v3
	v_cvt_pk_fp8_f32 v9, v5, v7
	s_waitcnt lgkmcnt(0)
	v_cvt_pk_fp8_f32 v9, v6, v8 op_sel:[0,0,1]
	v_add_co_u32_e32 v6, vcc, 0x5000, v68
	s_nop 1
	v_addc_co_u32_e32 v7, vcc, 0, v69, vcc
	global_store_dword v[6:7], v9, off

; __device__ __forceinline__ unsigned cvt4_fp8(float a, float b, float c, float d) { int w = 0; w = __builtin_amdgcn_cvt_pk_fp8_f32(a, b, w, false); w = __builtin_amdgcn_cvt_pk_fp8_f32(c, d, w, true); return (unsigned)w; }
; template <bool MLA>
; __device__ __forceinline__ void attn_unit(char* lds, int h, int qb, const bf16_t* Qp, int ldq, const bf16_t* Kp, int ldk, const bf16_t* KRp, const bf16_t* Vp, int ldv,
;                                           unsigned char* Op, int ldo, const float* KMp, const float* rel_bias) {
;     ...
;     for (int r = 0; r < 16; ++r) { const int orow = CROWC(r) + 4 * hi; const float rl = 16.0f * __builtin_amdgcn_rcpf(li_h[CROWC(r)]);
; #pragma unroll
;         for (int d0 = 0; d0 < 4; ++d0) { const float v = o[d0][r] * rl; const float v1 = __shfl_xor(v, 1), v2 = __shfl_xor(v, 2), v3 = __shfl_xor(v1, 2);
;             if ((r32 & 3) == 0) *(unsigned*)(Ow + (size_t)orow * ldo + d0 * 32 + r32) = cvt4_fp8(v, v1, v2, v3); } }
.LBB0_1703:
	s_or_b64 exec, exec, s[12:13]
	v_mov_b32_e32 v4, v240
	v_rcp_f32_e32 v4, v4
	s_nop 0
	v_mul_f32_e32 v4, 0x41800000, v4
	v_mul_f32_e32 v5, v59, v4
	s_nop 1
	v_mov_b32_dpp v7, v5 quad_perm:[1,0,3,2] row_mask:0xf bank_mask:0xf
	s_nop 1
	v_mov_b32_dpp v6, v5 quad_perm:[2,3,0,1] row_mask:0xf bank_mask:0xf
	s_waitcnt lgkmcnt(0)
	s_nop 1
	v_mov_b32_dpp v8, v7 quad_perm:[2,3,0,1] row_mask:0xf bank_mask:0xf
	s_and_saveexec_b64 s[12:13], s[6:7]
	s_cbranch_execz .LBB0_1705
	v_mov_b32_e32 v9, v3
	v_cvt_pk_fp8_f32 v9, v5, v7
	s_waitcnt lgkmcnt(0)
	v_cvt_pk_fp8_f32 v9, v6, v8 op_sel:[0,0,1]
	v_add_co_u32_e32 v6, vcc, 0x5000, v68
	s_nop 1
	v_addc_co_u32_e32 v7, vcc, 0, v69, vcc
	global_store_dword v[6:7], v9, off offset:2048

; __device__ __forceinline__ unsigned cvt4_fp8(float a, float b, float c, float d) { int w = 0; w = __builtin_amdgcn_cvt_pk_fp8_f32(a, b, w, false); w = __builtin_amdgcn_cvt_pk_fp8_f32(c, d, w, true); return (unsigned)w; }
; template <bool MLA>
; __device__ __forceinline__ void attn_unit(char* lds, int h, int qb, const bf16_t* Qp, int ldq, const bf16_t* Kp, int ldk, const bf16_t* KRp, const bf16_t* Vp, int ldv,
;                                           unsigned char* Op, int ldo, const float* KMp, const float* rel_bias) {
;     ...
;     for (int r = 0; r < 16; ++r) { const int orow = CROWC(r) + 4 * hi; const float rl = 16.0f * __builtin_amdgcn_rcpf(li_h[CROWC(r)]);
; #pragma unroll
;         for (int d0 = 0; d0 < 4; ++d0) { const float v = o[d0][r] * rl; const float v1 = __shfl_xor(v, 1), v2 = __shfl_xor(v, 2), v3 = __shfl_xor(v1, 2);
;             if ((r32 & 3) == 0) *(unsigned*)(Ow + (size_t)orow * ldo + d0 * 32 + r32) = cvt4_fp8(v, v1, v2, v3); } }
.LBB0_1711:
	s_or_b64 exec, exec, s[12:13]
	v_mov_b32_e32 v4, v241
	v_rcp_f32_e32 v4, v4
	s_nop 0
	v_mul_f32_e32 v4, 0x41800000, v4
	v_mul_f32_e32 v5, v60, v4
	s_nop 1
	v_mov_b32_dpp v7, v5 quad_perm:[1,0,3,2] row_mask:0xf bank_mask:0xf
	s_nop 1
	v_mov_b32_dpp v6, v5 quad_perm:[2,3,0,1] row_mask:0xf bank_mask:0xf
	s_waitcnt lgkmcnt(0)
	s_nop 1
	v_mov_b32_dpp v8, v7 quad_perm:[2,3,0,1] row_mask:0xf bank_mask:0xf
	s_and_saveexec_b64 s[12:13], s[6:7]
	s_cbranch_execz .LBB0_1713
	v_mov_b32_e32 v9, v3
	v_cvt_pk_fp8_f32 v9, v5, v7
	s_waitcnt lgkmcnt(0)
	v_cvt_pk_fp8_f32 v9, v6, v8 op_sel:[0,0,1]
	v_add_co_u32_e32 v6, vcc, 0x8000, v68
	s_nop 1
	v_addc_co_u32_e32 v7, vcc, 0, v69, vcc
	global_store_dword v[6:7], v9, off

; __device__ __forceinline__ unsigned cvt4_fp8(float a, float b, float c, float d) { int w = 0; w = __builtin_amdgcn_cvt_pk_fp8_f32(a, b, w, false); w = __builtin_amdgcn_cvt_pk_fp8_f32(c, d, w, true); return (unsigned)w; }
; template <bool MLA>
; __device__ __forceinline__ void attn_unit(char* lds, int h, int qb, const bf16_t* Qp, int ldq, const bf16_t* Kp, int ldk, const bf16_t* KRp, const bf16_t* Vp, int ldv,
;                                           unsigned char* Op, int ldo, const float* KMp, const float* rel_bias) {
;     ...
;     for (int r = 0; r < 16; ++r) { const int orow = CROWC(r) + 4 * hi; const float rl = 16.0f * __builtin_amdgcn_rcpf(li_h[CROWC(r)]);
; #pragma unroll
;         for (int d0 = 0; d0 < 4; ++d0) { const float v = o[d0][r] * rl; const float v1 = __shfl_xor(v, 1), v2 = __shfl_xor(v, 2), v3 = __shfl_xor(v1, 2);
;             if ((r32 & 3) == 0) *(unsigned*)(Ow + (size_t)orow * ldo + d0 * 32 + r32) = cvt4_fp8(v, v1, v2, v3); } }
.LBB0_1719:
	s_or_b64 exec, exec, s[12:13]
	v_mov_b32_e32 v4, v242
	v_rcp_f32_e32 v4, v4
	s_nop 0
	v_mul_f32_e32 v4, 0x41800000, v4
	v_mul_f32_e32 v5, v61, v4
	s_nop 1
	v_mov_b32_dpp v7, v5 quad_perm:[1,0,3,2] row_mask:0xf bank_mask:0xf
	s_nop 1
	v_mov_b32_dpp v6, v5 quad_perm:[2,3,0,1] row_mask:0xf bank_mask:0xf
	s_waitcnt lgkmcnt(0)
	s_nop 1
	v_mov_b32_dpp v8, v7 quad_perm:[2,3,0,1] row_mask:0xf bank_mask:0xf
	s_and_saveexec_b64 s[12:13], s[6:7]
	s_cbranch_execz .LBB0_1721
	v_mov_b32_e32 v9, v3
	v_cvt_pk_fp8_f32 v9, v5, v7
	s_waitcnt lgkmcnt(0)
	v_cvt_pk_fp8_f32 v9, v6, v8 op_sel:[0,0,1]
	v_add_co_u32_e32 v6, vcc, 0x8000, v68
	s_nop 1
	v_addc_co_u32_e32 v7, vcc, 0, v69, vcc
	global_store_dword v[6:7], v9, off offset:2048

; __device__ __forceinline__ unsigned cvt4_fp8(float a, float b, float c, float d) { int w = 0; w = __builtin_amdgcn_cvt_pk_fp8_f32(a, b, w, false); w = __builtin_amdgcn_cvt_pk_fp8_f32(c, d, w, true); return (unsigned)w; }
; template <bool MLA>
; __device__ __forceinline__ void attn_unit(char* lds, int h, int qb, const bf16_t* Qp, int ldq, const bf16_t* Kp, int ldk, const bf16_t* KRp, const bf16_t* Vp, int ldv,
;                                           unsigned char* Op, int ldo, const float* KMp, const float* rel_bias) {
;     ...
;     for (int r = 0; r < 16; ++r) { const int orow = CROWC(r) + 4 * hi; const float rl = 16.0f * __builtin_amdgcn_rcpf(li_h[CROWC(r)]);
; #pragma unroll
;         for (int d0 = 0; d0 < 4; ++d0) { const float v = o[d0][r] * rl; const float v1 = __shfl_xor(v, 1), v2 = __shfl_xor(v, 2), v3 = __shfl_xor(v1, 2);
;             if ((r32 & 3) == 0) *(unsigned*)(Ow + (size_t)orow * ldo + d0 * 32 + r32) = cvt4_fp8(v, v1, v2, v3); } }
.LBB0_1727:
	s_or_b64 exec, exec, s[12:13]
	v_mov_b32_e32 v4, v243
	v_rcp_f32_e32 v4, v4
	s_nop 0
	v_mul_f32_e32 v4, 0x41800000, v4
	v_mul_f32_e32 v5, v62, v4
	s_nop 1
	v_mov_b32_dpp v7, v5 quad_perm:[1,0,3,2] row_mask:0xf bank_mask:0xf
	s_nop 1
	v_mov_b32_dpp v6, v5 quad_perm:[2,3,0,1] row_mask:0xf bank_mask:0xf
	s_waitcnt lgkmcnt(0)
	s_nop 1
	v_mov_b32_dpp v8, v7 quad_perm:[2,3,0,1] row_mask:0xf bank_mask:0xf
	s_and_saveexec_b64 s[12:13], s[6:7]
	s_cbranch_execz .LBB0_1729
	v_mov_b32_e32 v9, v3
	v_cvt_pk_fp8_f32 v9, v5, v7
	s_waitcnt lgkmcnt(0)
	v_cvt_pk_fp8_f32 v9, v6, v8 op_sel:[0,0,1]
	v_add_co_u32_e32 v6, vcc, 0x9000, v68
	s_nop 1
	v_addc_co_u32_e32 v7, vcc, 0, v69, vcc
	global_store_dword v[6:7], v9, off

; __device__ __forceinline__ unsigned cvt4_fp8(float a, float b, float c, float d) { int w = 0; w = __builtin_amdgcn_cvt_pk_fp8_f32(a, b, w, false); w = __builtin_amdgcn_cvt_pk_fp8_f32(c, d, w, true); return (unsigned)w; }
; template <bool MLA>
; __device__ __forceinline__ void attn_unit(char* lds, int h, int qb, const bf16_t* Qp, int ldq, const bf16_t* Kp, int ldk, const bf16_t* KRp, const bf16_t* Vp, int ldv,
;                                           unsigned char* Op, int ldo, const float* KMp, const float* rel_bias) {
;     ...
;     for (int r = 0; r < 16; ++r) { const int orow = CROWC(r) + 4 * hi; const float rl = 16.0f * __builtin_amdgcn_rcpf(li_h[CROWC(r)]);
; #pragma unroll
;         for (int d0 = 0; d0 < 4; ++d0) { const float v = o[d0][r] * rl; const float v1 = __shfl_xor(v, 1), v2 = __shfl_xor(v, 2), v3 = __shfl_xor(v1, 2);
;             if ((r32 & 3) == 0) *(unsigned*)(Ow + (size_t)orow * ldo + d0 * 32 + r32) = cvt4_fp8(v, v1, v2, v3); } }
.LBB0_1735:
	s_or_b64 exec, exec, s[12:13]
	v_mov_b32_e32 v4, v244
	v_rcp_f32_e32 v4, v4
	s_nop 0
	v_mul_f32_e32 v4, 0x41800000, v4
	v_mul_f32_e32 v5, v63, v4
	s_nop 1
	v_mov_b32_dpp v7, v5 quad_perm:[1,0,3,2] row_mask:0xf bank_mask:0xf
	s_nop 1
	v_mov_b32_dpp v6, v5 quad_perm:[2,3,0,1] row_mask:0xf bank_mask:0xf
	s_waitcnt lgkmcnt(0)
	s_nop 1
	v_mov_b32_dpp v8, v7 quad_perm:[2,3,0,1] row_mask:0xf bank_mask:0xf
	s_and_saveexec_b64 s[12:13], s[6:7]
	s_cbranch_execz .LBB0_1737
	v_mov_b32_e32 v9, v3
	v_cvt_pk_fp8_f32 v9, v5, v7
	s_waitcnt lgkmcnt(0)
	v_cvt_pk_fp8_f32 v9, v6, v8 op_sel:[0,0,1]
	v_add_co_u32_e32 v6, vcc, 0x9000, v68
	s_nop 1
	v_addc_co_u32_e32 v7, vcc, 0, v69, vcc
	global_store_dword v[6:7], v9, off offset:2048

; __device__ __forceinline__ unsigned cvt4_fp8(float a, float b, float c, float d) { int w = 0; w = __builtin_amdgcn_cvt_pk_fp8_f32(a, b, w, false); w = __builtin_amdgcn_cvt_pk_fp8_f32(c, d, w, true); return (unsigned)w; }
; template <bool MLA>
; __device__ __forceinline__ void attn_unit(char* lds, int h, int qb, const bf16_t* Qp, int ldq, const bf16_t* Kp, int ldk, const bf16_t* KRp, const bf16_t* Vp, int ldv,
;                                           unsigned char* Op, int ldo, const float* KMp, const float* rel_bias) {
;     ...
;     for (int r = 0; r < 16; ++r) { const int orow = CROWC(r) + 4 * hi; const float rl = 16.0f * __builtin_amdgcn_rcpf(li_h[CROWC(r)]);
; #pragma unroll
;         for (int d0 = 0; d0 < 4; ++d0) { const float v = o[d0][r] * rl; const float v1 = __shfl_xor(v, 1), v2 = __shfl_xor(v, 2), v3 = __shfl_xor(v1, 2);
;             if ((r32 & 3) == 0) *(unsigned*)(Ow + (size_t)orow * ldo + d0 * 32 + r32) = cvt4_fp8(v, v1, v2, v3); } }
.LBB0_1743:
	s_or_b64 exec, exec, s[12:13]
	v_mov_b32_e32 v4, v245
	v_rcp_f32_e32 v4, v4
	s_nop 0
	v_mul_f32_e32 v4, 0x41800000, v4
	v_mul_f32_e32 v5, v64, v4
	s_nop 1
	v_mov_b32_dpp v7, v5 quad_perm:[1,0,3,2] row_mask:0xf bank_mask:0xf
	s_nop 1
	v_mov_b32_dpp v6, v5 quad_perm:[2,3,0,1] row_mask:0xf bank_mask:0xf
	s_waitcnt lgkmcnt(0)
	s_nop 1
	v_mov_b32_dpp v8, v7 quad_perm:[2,3,0,1] row_mask:0xf bank_mask:0xf
	s_and_saveexec_b64 s[12:13], s[6:7]
	s_cbranch_execz .LBB0_1745
	v_mov_b32_e32 v9, v3
	v_cvt_pk_fp8_f32 v9, v5, v7
	s_waitcnt lgkmcnt(0)
	v_cvt_pk_fp8_f32 v9, v6, v8 op_sel:[0,0,1]
	v_add_co_u32_e32 v6, vcc, 0xc000, v68
	s_nop 1
	v_addc_co_u32_e32 v7, vcc, 0, v69, vcc
	global_store_dword v[6:7], v9, off

; __device__ __forceinline__ unsigned cvt4_fp8(float a, float b, float c, float d) { int w = 0; w = __builtin_amdgcn_cvt_pk_fp8_f32(a, b, w, false); w = __builtin_amdgcn_cvt_pk_fp8_f32(c, d, w, true); return (unsigned)w; }
; template <bool MLA>
; __device__ __forceinline__ void attn_unit(char* lds, int h, int qb, const bf16_t* Qp, int ldq, const bf16_t* Kp, int ldk, const bf16_t* KRp, const bf16_t* Vp, int ldv,
;                                           unsigned char* Op, int ldo, const float* KMp, const float* rel_bias) {
;     ...
;     for (int r = 0; r < 16; ++r) { const int orow = CROWC(r) + 4 * hi; const float rl = 16.0f * __builtin_amdgcn_rcpf(li_h[CROWC(r)]);
; #pragma unroll
;         for (int d0 = 0; d0 < 4; ++d0) { const float v = o[d0][r] * rl; const float v1 = __shfl_xor(v, 1), v2 = __shfl_xor(v, 2), v3 = __shfl_xor(v1, 2);
;             if ((r32 & 3) == 0) *(unsigned*)(Ow + (size_t)orow * ldo + d0 * 32 + r32) = cvt4_fp8(v, v1, v2, v3); } }
.LBB0_1751:
	s_or_b64 exec, exec, s[12:13]
	v_mov_b32_e32 v4, v246
	v_rcp_f32_e32 v4, v4
	s_nop 0
	v_mul_f32_e32 v4, 0x41800000, v4
	v_mul_f32_e32 v5, v65, v4
	s_nop 1
	v_mov_b32_dpp v7, v5 quad_perm:[1,0,3,2] row_mask:0xf bank_mask:0xf
	s_nop 1
	v_mov_b32_dpp v6, v5 quad_perm:[2,3,0,1] row_mask:0xf bank_mask:0xf
	s_waitcnt lgkmcnt(0)
	s_nop 1
	v_mov_b32_dpp v8, v7 quad_perm:[2,3,0,1] row_mask:0xf bank_mask:0xf
	s_and_saveexec_b64 s[12:13], s[6:7]
	s_cbranch_execz .LBB0_1753
	v_mov_b32_e32 v9, v3
	v_cvt_pk_fp8_f32 v9, v5, v7
	s_waitcnt lgkmcnt(0)
	v_cvt_pk_fp8_f32 v9, v6, v8 op_sel:[0,0,1]
	v_add_co_u32_e32 v6, vcc, 0xc000, v68
	s_nop 1
	v_addc_co_u32_e32 v7, vcc, 0, v69, vcc
	global_store_dword v[6:7], v9, off offset:2048

; __device__ __forceinline__ unsigned cvt4_fp8(float a, float b, float c, float d) { int w = 0; w = __builtin_amdgcn_cvt_pk_fp8_f32(a, b, w, false); w = __builtin_amdgcn_cvt_pk_fp8_f32(c, d, w, true); return (unsigned)w; }
; template <bool MLA>
; __device__ __forceinline__ void attn_unit(char* lds, int h, int qb, const bf16_t* Qp, int ldq, const bf16_t* Kp, int ldk, const bf16_t* KRp, const bf16_t* Vp, int ldv,
;                                           unsigned char* Op, int ldo, const float* KMp, const float* rel_bias) {
;     ...
;     for (int r = 0; r < 16; ++r) { const int orow = CROWC(r) + 4 * hi; const float rl = 16.0f * __builtin_amdgcn_rcpf(li_h[CROWC(r)]);
; #pragma unroll
;         for (int d0 = 0; d0 < 4; ++d0) { const float v = o[d0][r] * rl; const float v1 = __shfl_xor(v, 1), v2 = __shfl_xor(v, 2), v3 = __shfl_xor(v1, 2);
;             if ((r32 & 3) == 0) *(unsigned*)(Ow + (size_t)orow * ldo + d0 * 32 + r32) = cvt4_fp8(v, v1, v2, v3); } }
.LBB0_1759:
	s_or_b64 exec, exec, s[12:13]
	v_mov_b32_e32 v4, v247
	v_rcp_f32_e32 v4, v4
	s_nop 0
	v_mul_f32_e32 v4, 0x41800000, v4
	v_mul_f32_e32 v5, v66, v4
	s_nop 1
	v_mov_b32_dpp v7, v5 quad_perm:[1,0,3,2] row_mask:0xf bank_mask:0xf
	s_nop 1
	v_mov_b32_dpp v6, v5 quad_perm:[2,3,0,1] row_mask:0xf bank_mask:0xf
	s_waitcnt lgkmcnt(0)
	s_nop 1
	v_mov_b32_dpp v8, v7 quad_perm:[2,3,0,1] row_mask:0xf bank_mask:0xf
	s_and_saveexec_b64 s[12:13], s[6:7]
	s_cbranch_execz .LBB0_1761
	v_mov_b32_e32 v9, v3
	v_cvt_pk_fp8_f32 v9, v5, v7
	s_waitcnt lgkmcnt(0)
	v_cvt_pk_fp8_f32 v9, v6, v8 op_sel:[0,0,1]
	v_add_co_u32_e32 v6, vcc, 0xd000, v68
	s_nop 1
	v_addc_co_u32_e32 v7, vcc, 0, v69, vcc
	global_store_dword v[6:7], v9, off

; __device__ __forceinline__ unsigned cvt4_fp8(float a, float b, float c, float d) { int w = 0; w = __builtin_amdgcn_cvt_pk_fp8_f32(a, b, w, false); w = __builtin_amdgcn_cvt_pk_fp8_f32(c, d, w, true); return (unsigned)w; }
; template <bool MLA>
; __device__ __forceinline__ void attn_unit(char* lds, int h, int qb, const bf16_t* Qp, int ldq, const bf16_t* Kp, int ldk, const bf16_t* KRp, const bf16_t* Vp, int ldv,
;                                           unsigned char* Op, int ldo, const float* KMp, const float* rel_bias) {
;     ...
;     for (int r = 0; r < 16; ++r) { const int orow = CROWC(r) + 4 * hi; const float rl = 16.0f * __builtin_amdgcn_rcpf(li_h[CROWC(r)]);
; #pragma unroll
;         for (int d0 = 0; d0 < 4; ++d0) { const float v = o[d0][r] * rl; const float v1 = __shfl_xor(v, 1), v2 = __shfl_xor(v, 2), v3 = __shfl_xor(v1, 2);
;             if ((r32 & 3) == 0) *(unsigned*)(Ow + (size_t)orow * ldo + d0 * 32 + r32) = cvt4_fp8(v, v1, v2, v3); } }
.LBB0_1767:
	s_or_b64 exec, exec, s[12:13]
	v_mov_b32_e32 v4, v248
	v_rcp_f32_e32 v4, v4
	s_nop 0
	v_mul_f32_e32 v4, 0x41800000, v4
	v_mul_f32_e32 v5, v67, v4
	s_nop 1
	v_mov_b32_dpp v7, v5 quad_perm:[1,0,3,2] row_mask:0xf bank_mask:0xf
	s_nop 1
	v_mov_b32_dpp v6, v5 quad_perm:[2,3,0,1] row_mask:0xf bank_mask:0xf
	s_waitcnt lgkmcnt(0)
	s_nop 1
	v_mov_b32_dpp v8, v7 quad_perm:[2,3,0,1] row_mask:0xf bank_mask:0xf
	s_and_saveexec_b64 s[12:13], s[6:7]
	s_cbranch_execz .LBB0_1769
	v_mov_b32_e32 v9, v3
	v_cvt_pk_fp8_f32 v9, v5, v7
	s_waitcnt lgkmcnt(0)
	v_cvt_pk_fp8_f32 v9, v6, v8 op_sel:[0,0,1]
	v_add_co_u32_e32 v6, vcc, 0xd000, v68
	s_nop 1
	v_addc_co_u32_e32 v7, vcc, 0, v69, vcc
	global_store_dword v[6:7], v9, off offset:2048
